# progress-based s_setprio in edge kernels + k_final rewrite + early z load + store-wait removal
# speedup vs baseline: 1.0642x; 1.0642x over previous
.LBB3_8:
	s_or_b64 exec, exec, s[2:3]
	s_movk_i32 s15, 0x61a8
	v_cmp_gt_i32_e32 vcc, s15, v56
	s_waitcnt lgkmcnt(0)
	s_barrier
	s_and_saveexec_b64 s[2:3], vcc
	s_cbranch_execz .LBB3_73
	s_load_dwordx4 s[16:19], s[0:1], 0x30
	v_and_b32_e32 v1, 63, v0
	s_waitcnt vmcnt(3)
	v_mov_b32_e32 v2, 0x3e020821
	v_cmp_gt_u32_e64 s[0:1], 32, v1
	v_mov_b32_e32 v65, 0xffff
	v_cmp_ne_u32_e32 vcc, 0, v52
	v_cndmask_b32_e64 v64, v2, 0, s[0:1]
	s_waitcnt vmcnt(0)
	v_lshrrev_b32_e32 v2, 16, v53
	v_lshrrev_b32_e32 v0, 1, v0
	v_mov_b32_e32 v3, 0x7a00
	v_ashrrev_i32_e32 v57, 31, v56
	v_cndmask_b32_e32 v77, v65, v2, vcc
	s_lshl_b32 s6, s6, 2
	v_lshlrev_b32_e32 v2, 4, v1
	v_and_or_b32 v67, v0, 16, v3
	v_lshlrev_b32_e32 v70, 1, v1
	v_lshlrev_b32_e32 v36, 2, v1
	v_lshlrev_b64 v[0:1], 8, v[56:57]
	v_mov_b32_e32 v37, 0
	v_or_b32_e32 v0, v0, v36
	s_ashr_i32 s7, s6, 31
	s_mov_b32 s5, 0
	v_add_u32_e32 v66, 0x3200, v2
	v_add_u32_e32 v68, 0x5200, v2
	v_add_u32_e32 v69, 0x7200, v2
	s_waitcnt lgkmcnt(0)
	v_lshl_add_u64 v[58:59], s[16:17], 0, v[36:37]
	v_lshl_add_u64 v[60:61], s[18:19], 0, v[0:1]
	s_lshl_b64 s[10:11], s[6:7], 8
	s_mov_b64 s[12:13], 0
	s_movk_i32 s7, 0x61a7
	v_mov_b32_e32 v57, 0xc0669d92
	s_mov_b32 s20, 0xc1c00000
	v_mov_b32_e32 v71, 0x41c00000
	v_mov_b32_e32 v72, 0xbfb8aa3b
	v_mov_b32_e32 v73, 0xc1b69213
	v_mov_b32_e32 v74, 0xc228283a
	v_mov_b32_e32 v75, 0xc275076b
	s_mov_b32 s14, 0x3e0a9555
	s_mov_b32 s94, 0
	s_branch .LBB3_11
.LBB3_10:
	s_and_b64 s[2:3], exec, s[2:3]
	s_or_b64 s[12:13], s[2:3], s[12:13]
	v_readlane_b32 s2, v34, 31
	s_bfe_u32 s3, s2, 0x80008
	v_lshl_or_b32 v2, s3, 7, v70
	ds_read_u16 v2, v2
	s_bfe_u32 s2, s2, 0x100010
	v_add_f32_e32 v1, v1, v15
	s_waitcnt lgkmcnt(1)
	v_fma_mix_f32 v0, v15, v35, v0 op_sel_hi:[0,1,0]
	s_lshl_b32 s4, s2, 8
	s_waitcnt lgkmcnt(0)
	v_fma_mix_f32 v2, v2, v1, v0 op_sel_hi:[1,0,0]
	v_lshl_add_u64 v[0:1], v[58:59], 0, s[4:5]
	s_nop 0
	v_cndmask_b32_sdwa v77, v76, v65, vcc dst_sel:DWORD dst_unused:UNUSED_PAD src0_sel:WORD_1 src1_sel:DWORD
	v_cndmask_b32_e64 v1, v61, v1, s[18:19]
	v_cndmask_b32_e64 v0, v60, v0, s[18:19]
	v_lshl_add_u64 v[60:61], v[60:61], 0, s[10:11]
	v_mov_b64_e32 v[32:33], v[40:41]
	v_mov_b64_e32 v[34:35], v[42:43]
	global_store_dword v[0:1], v2, off sc1
	s_andn2_b64 exec, exec, s[12:13]
	s_cbranch_execz .LBB3_73
.LBB3_11:
	s_cmp_lt_u32 s94, 4
	s_cbranch_scc1 .Lprio_e0_3
	s_cmp_lt_u32 s94, 5
	s_cbranch_scc1 .Lprio_e0_2
	s_cmp_lt_u32 s94, 6
	s_cbranch_scc1 .Lprio_e0_1
	s_setprio 0
	s_branch .Lprio_e0_done
.Lprio_e0_3:
	s_setprio 3
	s_branch .Lprio_e0_done
.Lprio_e0_2:
	s_setprio 2
	s_branch .Lprio_e0_done
.Lprio_e0_1:
	s_setprio 1
.Lprio_e0_done:
	s_add_u32 s94, s94, 1
	v_sub_f32_e32 v36, v32, v64
	v_fmamk_f32 v38, v36, 0x4297576a, v57
	v_fmamk_f32 v39, v36, 0x4297576a, v73
	v_med3_f32 v41, v38, s20, v71
	v_med3_f32 v43, v39, s20, v71
	v_mul_f32_e64 v38, v41, -v41
	v_mul_f32_e64 v39, v43, -v43
	v_exp_f32_e32 v38, v38
	v_exp_f32_e32 v39, v39
	v_fmamk_f32 v40, v41, 0x4019be61, v72
	v_fmamk_f32 v41, v41, 0xc019be61, v72
	v_exp_f32_e32 v42, v41
	v_pk_mul_f32 v[46:47], v[32:33], v[38:39] op_sel:[1,0]
	v_fmamk_f32 v38, v43, 0x4019be61, v72
	v_exp_f32_e32 v41, v38
	v_fmamk_f32 v38, v43, 0xc019be61, v72
	v_exp_f32_e32 v43, v38
	v_fmamk_f32 v38, v36, 0x4297576a, v74
	v_fmamk_f32 v36, v36, 0x4297576a, v75
	v_med3_f32 v45, v38, s20, v71
	v_med3_f32 v36, v36, s20, v71
	v_mul_f32_e64 v38, v45, -v45
	v_mul_f32_e64 v39, v36, -v36
	v_exp_f32_e32 v38, v38
	v_exp_f32_e32 v39, v39
	v_exp_f32_e32 v40, v40
	v_fmamk_f32 v44, v45, 0x4019be61, v72
	v_fmamk_f32 v45, v45, 0xc019be61, v72
	v_pk_mul_f32 v[54:55], v[32:33], v[38:39] op_sel:[1,0]
	v_fmamk_f32 v38, v36, 0x4019be61, v72
	v_exp_f32_e32 v48, v45
	v_exp_f32_e32 v45, v38
	v_pk_mul_f32 v[50:51], v[40:41], v[46:47]
	v_pk_mul_f32 v[38:39], v[40:41], s[14:15] op_sel_hi:[1,0]
	v_exp_f32_e32 v44, v44
	v_pk_mul_f32 v[52:53], v[38:39], v[50:51]
	v_pk_mul_f32 v[38:39], v[38:39], s[14:15] op_sel_hi:[1,0]
	ds_read_b128 v[12:15], v66
	ds_read_b128 v[8:11], v66 offset:1024
	ds_read_b128 v[4:7], v66 offset:2048
	ds_read_b128 v[0:3], v66 offset:3072
	ds_read_b128 v[16:19], v67
	ds_read_b128 v[20:23], v67 offset:32
	ds_read_b128 v[24:27], v67 offset:64
	ds_read_b128 v[28:31], v67 offset:96
	v_pk_mul_f32 v[78:79], v[38:39], v[52:53]
	v_pk_mul_f32 v[38:39], v[38:39], s[14:15] op_sel_hi:[1,0]
	v_pk_mul_f32 v[82:83], v[42:43], v[46:47]
	v_pk_mul_f32 v[80:81], v[38:39], v[78:79]
	v_pk_mul_f32 v[38:39], v[42:43], s[14:15] op_sel_hi:[1,0]
	v_pk_mul_f32 v[86:87], v[44:45], v[54:55]
	v_pk_mul_f32 v[42:43], v[38:39], v[82:83]
	v_pk_mul_f32 v[38:39], v[38:39], s[14:15] op_sel_hi:[1,0]
	v_cvt_pk_f16_f32 v40, v50, v52
	v_pk_mul_f32 v[84:85], v[38:39], v[42:43]
	v_pk_mul_f32 v[38:39], v[44:45], s[14:15] op_sel_hi:[1,0]
	v_cvt_pk_f16_f32 v41, v78, v80
	v_pk_mul_f32 v[88:89], v[38:39], v[86:87]
	v_pk_mul_f32 v[38:39], v[38:39], s[14:15] op_sel_hi:[1,0]
	v_fmamk_f32 v36, v36, 0xc019be61, v72
	v_pk_mul_f32 v[90:91], v[38:39], v[88:89]
	v_pk_mul_f32 v[44:45], v[38:39], s[14:15] op_sel_hi:[1,0]
	v_cvt_pk_f16_f32 v38, v84, v42
	v_cvt_pk_f16_f32 v39, v82, v46
	v_cvt_pk_f16_f32 v42, v85, v43
	v_cvt_pk_f16_f32 v43, v83, v47
	s_waitcnt lgkmcnt(0)
	v_mfma_f32_32x32x16_f16 v[16:31], v[12:15], v[38:41], v[16:31]
	v_mul_f32_e64 v12, v44, v90
	v_mul_f32_e64 v13, v45, v91
	v_cvt_pk_f16_f32 v44, v51, v53
	v_cvt_pk_f16_f32 v45, v79, v81
	v_exp_f32_e32 v49, v36
	ds_read_b128 v[50:53], v66 offset:4096
	v_cvt_pk_f16_f32 v82, v87, v89
	v_cvt_pk_f16_f32 v83, v91, v13
	v_mfma_f32_32x32x16_f16 v[16:31], v[8:11], v[42:45], v[16:31]
	v_mul_f32_e64 v14, v48, v54
	v_mul_f32_e64 v15, v49, v55
	v_mul_f32_e64 v48, v48, s14
	v_mul_f32_e64 v49, v49, s14
	v_cvt_pk_f16_f32 v47, v14, v54
	v_pk_mul_f32 v[8:9], v[48:49], v[14:15]
	v_pk_mul_f32 v[10:11], v[48:49], s[14:15] op_sel_hi:[1,0]
	v_cvt_pk_f16_f32 v48, v86, v88
	v_pk_mul_f32 v[10:11], v[10:11], v[8:9]
	v_cvt_pk_f16_f32 v49, v90, v12
	v_cvt_pk_f16_f32 v46, v10, v8
	v_cvt_pk_f16_f32 v80, v11, v9
	v_cvt_pk_f16_f32 v81, v15, v55
	v_mfma_f32_32x32x16_f16 v[16:31], v[4:7], v[46:49], v[16:31]
	v_mov_b32_e32 v36, v56
	v_add_u32_e32 v56, s6, v36
	v_cmp_gt_i32_e32 vcc, s15, v56
	v_mov_b32_e32 v78, v63
	v_readlane_b32 s21, v35, 0
	v_cndmask_b32_e32 v36, v36, v56, vcc
	v_cmp_ne_u32_sdwa s[16:17], v78, v34 src0_sel:WORD_1 src1_sel:WORD_1
	v_mfma_f32_32x32x16_f16 v[16:31], v[0:3], v[80:83], v[16:31]
	ds_read_b128 v[0:3], v67 offset:128
	ds_read_b128 v[4:7], v67 offset:160
	ds_read_b128 v[8:11], v67 offset:192
	ds_read_b128 v[12:15], v67 offset:224
	ds_read_b128 v[84:87], v66 offset:5120
	v_min_f32 v16, 0x42fc0000, v16
	v_min_f32 v17, 0x42fc0000, v17
	v_min_f32 v18, 0x42fc0000, v18
	v_min_f32 v19, 0x42fc0000, v19
	v_min_f32 v20, 0x42fc0000, v20
	v_min_f32 v21, 0x42fc0000, v21
	s_waitcnt lgkmcnt(1)
	v_mfma_f32_32x32x16_f16 v[0:15], v[50:53], v[38:41], v[0:15]
	ds_read_b128 v[38:41], v66 offset:6144
	ds_read_b128 v[50:53], v66 offset:7168
	v_min_f32 v22, 0x42fc0000, v22
	v_min_f32 v23, 0x42fc0000, v23
	s_nop 2
	v_exp_f32_e32 v16, v16
	v_exp_f32_e32 v17, v17
	v_exp_f32_e32 v18, v18
	s_waitcnt lgkmcnt(2)
	v_mfma_f32_32x32x16_f16 v[0:15], v[84:87], v[42:45], v[0:15]
	v_exp_f32_e32 v19, v19
	v_exp_f32_e32 v20, v20
	v_exp_f32_e32 v21, v21
	v_exp_f32_e32 v22, v22
	v_exp_f32_e32 v23, v23
	v_pk_add_f32 v[16:17], v[16:17], 1.0 op_sel_hi:[1,0]
	v_pk_add_f32 v[18:19], v[18:19], 1.0 op_sel_hi:[1,0]
	s_waitcnt lgkmcnt(1)
	v_mfma_f32_32x32x16_f16 v[0:15], v[38:41], v[46:49], v[0:15]
	v_add_f32_e64 v20, v20, 1.0
	v_add_f32_e64 v21, v21, 1.0
	v_add_f32_e64 v22, v22, 1.0
	v_add_f32_e64 v23, v23, 1.0
	v_log_f32_e32 v16, v16
	v_log_f32_e32 v17, v17
	v_log_f32_e32 v18, v18
	v_log_f32_e32 v19, v19
	v_log_f32_e32 v20, v20
	s_waitcnt lgkmcnt(0)
	v_mfma_f32_32x32x16_f16 v[0:15], v[50:53], v[80:83], v[0:15]
	v_min_f32 v6, 0x42fc0000, v6
	v_min_f32 v7, 0x42fc0000, v7
	v_min_f32 v0, 0x42fc0000, v0
	v_min_f32 v1, 0x42fc0000, v1
	v_min_f32 v4, 0x42fc0000, v4
	v_min_f32 v5, 0x42fc0000, v5
	s_nop 11
	v_exp_f32_e32 v6, v6
	v_exp_f32_e32 v7, v7
	v_exp_f32_e32 v0, v0
	v_exp_f32_e32 v1, v1
	v_log_f32_e32 v21, v21
	v_pk_add_f32 v[6:7], v[6:7], 1.0 op_sel_hi:[1,0]
	v_log_f32_e32 v22, v22
	v_log_f32_e32 v6, v6
	v_log_f32_e32 v7, v7
	v_log_f32_e32 v23, v23
	v_min_f32 v2, 0x42fc0000, v2
	v_min_f32 v3, 0x42fc0000, v3
	v_exp_f32_e32 v4, v4
	v_exp_f32_e32 v5, v5
	v_lshl_or_b32 v42, v36, 5, v62
	v_exp_f32_e32 v2, v2
	v_exp_f32_e32 v3, v3
	v_cmp_eq_u32_e32 vcc, 0, v42
	v_pk_add_f32 v[0:1], v[0:1], 1.0 op_sel_hi:[1,0]
	v_pk_mul_f32 v[6:7], v[32:33], v[6:7] op_sel:[1,0]
	v_ashrrev_i32_e32 v43, 31, v42
	v_cndmask_b32_e64 v36, 0, 1, vcc
	v_log_f32_e32 v0, v0
	v_log_f32_e32 v1, v1
	v_cvt_pk_f16_f32 v55, v6, v7
	v_min_f32 v6, 0x42fc0000, v10
	v_min_f32 v7, 0x42fc0000, v11
	v_lshl_add_u64 v[44:45], v[42:43], 4, s[8:9]
	v_lshlrev_b32_e32 v36, 4, v36
	v_pk_mul_f32 v[16:17], v[32:33], v[16:17] op_sel:[1,0]
	v_pk_mul_f32 v[18:19], v[32:33], v[18:19] op_sel:[1,0]
	v_pk_mul_f32 v[20:21], v[32:33], v[20:21] op_sel:[1,0]
	v_pk_mul_f32 v[22:23], v[32:33], v[22:23] op_sel:[1,0]
	v_pk_add_f32 v[4:5], v[4:5], 1.0 op_sel_hi:[1,0]
	v_exp_f32_e32 v6, v6
	v_exp_f32_e32 v7, v7
	v_lshl_add_u64 v[38:39], v[44:45], 0, v[36:37]
	global_load_dwordx4 v[40:43], v[44:45], off
	global_load_dword v63, v[44:45], off offset:24
	global_load_dword v76, v[38:39], off offset:-8
	v_cvt_pk_f16_f32 v47, v22, v23
	v_cvt_pk_f16_f32 v46, v20, v21
	v_cvt_pk_f16_f32 v45, v18, v19
	v_cvt_pk_f16_f32 v44, v16, v17
	v_min_f32 v16, 0x42fc0000, v24
	v_min_f32 v17, 0x42fc0000, v25
	v_min_f32 v18, 0x42fc0000, v26
	v_min_f32 v19, 0x42fc0000, v27
	v_min_f32 v20, 0x42fc0000, v28
	v_min_f32 v21, 0x42fc0000, v29
	v_min_f32 v22, 0x42fc0000, v30
	v_min_f32 v23, 0x42fc0000, v31
	v_pk_add_f32 v[2:3], v[2:3], 1.0 op_sel_hi:[1,0]
	v_log_f32_e32 v4, v4
	v_log_f32_e32 v5, v5
	v_min_f32 v8, 0x42fc0000, v8
	v_min_f32 v9, 0x42fc0000, v9
	v_exp_f32_e32 v16, v16
	v_exp_f32_e32 v17, v17
	v_exp_f32_e32 v18, v18
	v_exp_f32_e32 v19, v19
	v_exp_f32_e32 v20, v20
	v_exp_f32_e32 v21, v21
	v_exp_f32_e32 v22, v22
	v_exp_f32_e32 v23, v23
	v_log_f32_e32 v2, v2
	v_log_f32_e32 v3, v3
	v_exp_f32_e32 v8, v8
	v_exp_f32_e32 v9, v9
	v_pk_mul_f32 v[0:1], v[32:33], v[0:1] op_sel:[1,0]
	v_pk_mul_f32 v[4:5], v[32:33], v[4:5] op_sel:[1,0]
	v_cvt_pk_f16_f32 v52, v0, v1
	v_pk_add_f32 v[0:1], v[6:7], 1.0 op_sel_hi:[1,0]
	v_pk_add_f32 v[16:17], v[16:17], 1.0 op_sel_hi:[1,0]
	v_log_f32_e32 v10, v0
	v_min_f32 v0, 0x42fc0000, v12
	v_pk_add_f32 v[18:19], v[18:19], 1.0 op_sel_hi:[1,0]
	v_pk_add_f32 v[20:21], v[20:21], 1.0 op_sel_hi:[1,0]
	v_pk_add_f32 v[22:23], v[22:23], 1.0 op_sel_hi:[1,0]
	v_pk_mul_f32 v[2:3], v[32:33], v[2:3] op_sel:[1,0]
	v_cvt_pk_f16_f32 v54, v4, v5
	v_pk_add_f32 v[4:5], v[8:9], 1.0 op_sel_hi:[1,0]
	v_exp_f32_e32 v12, v0
	v_min_f32 v0, 0x42fc0000, v13
	v_log_f32_e32 v16, v16
	v_log_f32_e32 v17, v17
	v_log_f32_e32 v18, v18
	v_log_f32_e32 v19, v19
	v_log_f32_e32 v20, v20
	v_log_f32_e32 v21, v21
	v_log_f32_e32 v22, v22
	v_log_f32_e32 v23, v23
	v_log_f32_e32 v4, v4
	v_log_f32_e32 v5, v5
	v_cvt_pk_f16_f32 v53, v2, v3
	v_log_f32_e32 v11, v1
	v_exp_f32_e32 v13, v0
	ds_read_b128 v[0:3], v68
	v_pk_mul_f32 v[16:17], v[32:33], v[16:17] op_sel:[1,0]
	v_pk_mul_f32 v[18:19], v[32:33], v[18:19] op_sel:[1,0]
	v_pk_mul_f32 v[20:21], v[32:33], v[20:21] op_sel:[1,0]
	v_pk_mul_f32 v[22:23], v[32:33], v[22:23] op_sel:[1,0]
	v_pk_mul_f32 v[8:9], v[32:33], v[4:5] op_sel:[1,0]
	v_min_f32 v4, 0x42fc0000, v14
	v_cvt_pk_f16_f32 v51, v22, v23
	v_cvt_pk_f16_f32 v50, v20, v21
	v_cvt_pk_f16_f32 v49, v18, v19
	v_cvt_pk_f16_f32 v48, v16, v17
	v_exp_f32_e32 v14, v4
	ds_read_b128 v[4:7], v68 offset:1024
	s_waitcnt lgkmcnt(1)
	v_mfma_f32_32x32x16_f16 v[16:31], v[44:47], v[0:3], 0
	v_min_f32 v15, 0x42fc0000, v15
	v_add_f32_e64 v0, v12, 1.0
	v_add_f32_e64 v1, v13, 1.0
	v_exp_f32_e32 v15, v15
	v_log_f32_e32 v0, v0
	v_log_f32_e32 v1, v1
	v_pk_mul_f32 v[10:11], v[32:33], v[10:11] op_sel:[1,0]
	v_pk_add_f32 v[2:3], v[14:15], 1.0 op_sel_hi:[1,0]
	s_waitcnt lgkmcnt(0)
	v_mfma_f32_32x32x16_f16 v[16:31], v[48:51], v[4:7], v[16:31]
	v_log_f32_e32 v12, v2
	v_log_f32_e32 v13, v3
	v_pk_mul_f32 v[4:5], v[32:33], v[0:1] op_sel:[1,0]
	ds_read_b128 v[0:3], v68 offset:2048
	v_cvt_pk_f16_f32 v82, v4, v5
	v_pk_mul_f32 v[6:7], v[32:33], v[12:13] op_sel:[1,0]
	v_cvt_pk_f16_f32 v81, v10, v11
	v_cvt_pk_f16_f32 v83, v6, v7
	ds_read_b128 v[4:7], v68 offset:3072
	s_waitcnt lgkmcnt(1)
	v_mfma_f32_32x32x16_f16 v[16:31], v[52:55], v[0:3], v[16:31]
	v_cvt_pk_f16_f32 v80, v8, v9
	v_cvt_f16_f32_e32 v0, v33
	v_mov_b32_e32 v38, v37
	v_mov_b32_e32 v39, v37
	ds_read_b128 v[84:87], v69 offset:1024
	v_cndmask_b32_e64 v0, 0, v0, s[0:1]
	v_pack_b32_f16 v36, v0, 0
	s_waitcnt lgkmcnt(1)
	v_mfma_f32_32x32x16_f16 v[16:31], v[80:83], v[4:7], v[16:31]
	ds_read_b128 v[0:3], v69
	ds_read_b128 v[88:91], v68 offset:5120
	s_ashr_i32 s17, s21, 9
	v_readlane_b32 s22, v35, 1
	s_and_b32 s17, s17, 0xffffff80
	v_or_b32_e32 v32, s17, v70
	s_ashr_i32 s17, s22, 9
	s_waitcnt lgkmcnt(1)
	v_mfma_f32_32x32x16_f16 v[16:31], v[36:39], v[0:3], v[16:31]
	ds_read_b128 v[0:3], v68 offset:4096
	v_readlane_b32 s23, v35, 2
	s_and_b32 s17, s17, 0xffffff80
	v_or_b32_e32 v33, s17, v70
	s_ashr_i32 s17, s23, 9
	v_readlane_b32 s24, v35, 3
	s_and_b32 s17, s17, 0xffffff80
	s_waitcnt lgkmcnt(0)
	v_mfma_f32_32x32x16_f16 v[0:15], v[44:47], v[0:3], 0
	ds_read_b128 v[44:47], v68 offset:6144
	v_readlane_b32 s25, v35, 4
	v_readlane_b32 s26, v35, 5
	v_readlane_b32 s27, v35, 6
	v_readlane_b32 s28, v35, 7
	v_readlane_b32 s29, v35, 8
	v_readlane_b32 s30, v35, 9
	v_mfma_f32_32x32x16_f16 v[0:15], v[48:51], v[88:91], v[0:15]
	ds_read_b128 v[48:51], v68 offset:7168
	v_readlane_b32 s31, v35, 10
	v_readlane_b32 s33, v35, 11
	v_readlane_b32 s34, v35, 12
	v_readlane_b32 s35, v35, 13
	v_readlane_b32 s36, v35, 14
	v_readlane_b32 s37, v35, 15
	s_waitcnt lgkmcnt(1)
	v_mfma_f32_32x32x16_f16 v[0:15], v[52:55], v[44:47], v[0:15]
	v_readlane_b32 s38, v35, 16
	v_readlane_b32 s39, v35, 17
	v_readlane_b32 s40, v35, 18
	v_readlane_b32 s41, v35, 19
	v_readlane_b32 s42, v35, 20
	v_readlane_b32 s43, v35, 21
	v_readlane_b32 s44, v35, 22
	s_waitcnt lgkmcnt(0)
	v_mfma_f32_32x32x16_f16 v[0:15], v[80:83], v[48:51], v[0:15]
	v_readlane_b32 s45, v35, 23
	v_readlane_b32 s46, v35, 24
	v_readlane_b32 s47, v35, 25
	v_readlane_b32 s48, v35, 26
	v_readlane_b32 s49, v35, 27
	v_readlane_b32 s50, v35, 28
	v_readlane_b32 s51, v35, 29
	v_readlane_b32 s52, v35, 30
	v_readlane_b32 s4, v35, 31
	v_or_b32_e32 v35, s17, v70
	s_ashr_i32 s17, s24, 9
	s_and_b32 s17, s17, 0xffffff80
	v_mfma_f32_32x32x16_f16 v[0:15], v[36:39], v[84:87], v[0:15]
	v_or_b32_e32 v36, s17, v70
	s_ashr_i32 s17, s25, 9
	s_and_b32 s17, s17, 0xffffff80
	v_or_b32_e32 v38, s17, v70
	s_ashr_i32 s17, s26, 9
	s_and_b32 s17, s17, 0xffffff80
	v_or_b32_e32 v39, s17, v70
	s_ashr_i32 s17, s27, 9
	s_and_b32 s17, s17, 0xffffff80
	v_or_b32_e32 v44, s17, v70
	s_ashr_i32 s17, s28, 9
	s_and_b32 s17, s17, 0xffffff80
	v_or_b32_e32 v45, s17, v70
	s_ashr_i32 s17, s29, 9
	s_and_b32 s17, s17, 0xffffff80
	ds_read_u16 v32, v32
	ds_read_u16 v91, v33
	ds_read_u16 v90, v35
	ds_read_u16 v89, v36
	ds_read_u16 v88, v38
	ds_read_u16 v87, v39
	ds_read_u16 v86, v44
	ds_read_u16 v85, v45
	v_or_b32_e32 v33, s17, v70
	s_ashr_i32 s17, s30, 9
	s_and_b32 s17, s17, 0xffffff80
	v_or_b32_e32 v35, s17, v70
	s_ashr_i32 s17, s31, 9
	s_and_b32 s17, s17, 0xffffff80
	v_or_b32_e32 v36, s17, v70
	s_ashr_i32 s17, s33, 9
	s_and_b32 s17, s17, 0xffffff80
	v_or_b32_e32 v38, s17, v70
	s_ashr_i32 s17, s34, 9
	s_and_b32 s17, s17, 0xffffff80
	v_or_b32_e32 v39, s17, v70
	s_ashr_i32 s17, s35, 9
	s_and_b32 s17, s17, 0xffffff80
	v_or_b32_e32 v44, s17, v70
	s_ashr_i32 s17, s36, 9
	s_and_b32 s17, s17, 0xffffff80
	v_or_b32_e32 v45, s17, v70
	s_ashr_i32 s17, s37, 9
	s_and_b32 s17, s17, 0xffffff80
	v_or_b32_e32 v46, s17, v70
	s_ashr_i32 s17, s38, 9
	s_and_b32 s17, s17, 0xffffff80
	v_cmp_ne_u32_sdwa s[18:19], v77, v34 src0_sel:DWORD src1_sel:WORD_1
	ds_read_u16 v84, v33
	ds_read_u16 v83, v35
	ds_read_u16 v82, v36
	ds_read_u16 v81, v38
	ds_read_u16 v80, v39
	ds_read_u16 v79, v44
	ds_read_u16 v78, v45
	ds_read_u16 v77, v46
	v_or_b32_e32 v33, s17, v70
	s_ashr_i32 s17, s39, 9
	s_and_b32 s17, s17, 0xffffff80
	v_or_b32_e32 v35, s17, v70
	s_ashr_i32 s17, s40, 9
	s_and_b32 s17, s17, 0xffffff80
	v_or_b32_e32 v36, s17, v70
	s_ashr_i32 s17, s41, 9
	s_and_b32 s17, s17, 0xffffff80
	v_or_b32_e32 v38, s17, v70
	s_ashr_i32 s17, s42, 9
	s_and_b32 s17, s17, 0xffffff80
	v_or_b32_e32 v39, s17, v70
	s_ashr_i32 s17, s43, 9
	s_and_b32 s17, s17, 0xffffff80
	v_or_b32_e32 v44, s17, v70
	s_ashr_i32 s17, s44, 9
	s_and_b32 s17, s17, 0xffffff80
	v_or_b32_e32 v45, s17, v70
	s_ashr_i32 s17, s45, 9
	s_and_b32 s17, s17, 0xffffff80
	v_or_b32_e32 v46, s17, v70
	s_ashr_i32 s17, s46, 9
	s_and_b32 s17, s17, 0xffffff80
	ds_read_u16 v55, v33
	ds_read_u16 v54, v35
	ds_read_u16 v53, v36
	ds_read_u16 v52, v38
	ds_read_u16 v51, v39
	ds_read_u16 v50, v44
	ds_read_u16 v49, v45
	ds_read_u16 v48, v46
	v_or_b32_e32 v33, s17, v70
	s_ashr_i32 s17, s47, 9
	s_and_b32 s17, s17, 0xffffff80
	v_or_b32_e32 v35, s17, v70
	s_ashr_i32 s17, s48, 9
	s_and_b32 s17, s17, 0xffffff80
	v_or_b32_e32 v36, s17, v70
	s_ashr_i32 s17, s49, 9
	s_and_b32 s17, s17, 0xffffff80
	v_or_b32_e32 v38, s17, v70
	s_ashr_i32 s17, s50, 9
	s_and_b32 s17, s17, 0xffffff80
	v_or_b32_e32 v39, s17, v70
	s_ashr_i32 s17, s51, 9
	s_and_b32 s17, s17, 0xffffff80
	v_or_b32_e32 v92, s17, v70
	s_ashr_i32 s17, s52, 9
	s_and_b32 s17, s17, 0xffffff80
	v_or_b32_e32 v93, s17, v70
	ds_read_u16 v47, v33
	ds_read_u16 v46, v35
	ds_read_u16 v45, v36
	ds_read_u16 v44, v38
	ds_read_u16 v39, v39
	ds_read_u16 v38, v92
	ds_read_u16 v36, v93
	s_ashr_i32 s4, s4, 9
	s_and_b32 s4, s4, 0xffffff80
	s_waitcnt lgkmcnt(14)
	v_cvt_f32_f16_e32 v32, v32
	v_or_b32_e32 v33, s4, v70
	ds_read_u16 v35, v33
	s_waitcnt vmcnt(0)
	v_permlane32_swap_b32_e32 v16, v0
	s_bitcmp1_b32 s18, 0
	v_mul_f32_e32 v32, v16, v32
	v_mov_b32_e32 v33, v16
	v_cmp_lt_i32_e64 s[2:3], s7, v56
	v_permlane32_swap_b32_e32 v17, v1
	v_permlane32_swap_b32_e32 v18, v2
	v_permlane32_swap_b32_e32 v19, v3
	v_permlane32_swap_b32_e32 v20, v4
	v_permlane32_swap_b32_e32 v21, v5
	v_permlane32_swap_b32_e32 v22, v6
	v_permlane32_swap_b32_e32 v23, v7
	v_permlane32_swap_b32_e32 v24, v8
	v_permlane32_swap_b32_e32 v25, v9
	v_permlane32_swap_b32_e32 v26, v10
	v_permlane32_swap_b32_e32 v27, v11
	v_permlane32_swap_b32_e32 v28, v12
	v_permlane32_swap_b32_e32 v29, v13
	v_permlane32_swap_b32_e32 v30, v14
	v_permlane32_swap_b32_e32 v31, v15
	s_cselect_b64 s[18:19], -1, 0
	s_bitcmp0_b32 s16, 0
	v_pk_add_f32 v[32:33], v[32:33], 0 op_sel_hi:[1,0]
	s_cbranch_scc1 .LBB3_13
	v_readlane_b32 s4, v34, 0
	s_bfe_u32 s17, s4, 0x80008
	v_lshl_or_b32 v16, s17, 7, v70
	ds_read_u16 v16, v16
	s_bfe_u32 s4, s4, 0x100010
	s_lshl_b32 s4, s4, 8
	v_lshl_add_u64 v[92:93], v[58:59], 0, s[4:5]
	v_cndmask_b32_e64 v93, v61, v93, s[18:19]
	s_waitcnt lgkmcnt(0)
	v_fma_mix_f32 v16, v16, v33, v32 op_sel_hi:[1,0,0]
	v_mov_b32_e32 v32, 0
	v_cndmask_b32_e64 v92, v60, v92, s[18:19]
	s_mov_b64 s[18:19], -1
	v_mov_b32_e32 v33, v32
	global_store_dword v[92:93], v16, off sc1

.LBB4_8:
	s_or_b64 exec, exec, s[2:3]
	s_movk_i32 s17, 0x61a8
	v_cmp_gt_i32_e32 vcc, s17, v64
	s_waitcnt lgkmcnt(0)
	s_barrier
	s_and_saveexec_b64 s[2:3], vcc
	s_cbranch_execz .LBB4_73
	s_load_dwordx4 s[4:7], s[0:1], 0x30
	s_load_dwordx2 s[2:3], s[0:1], 0x40
	v_and_b32_e32 v1, 63, v0
	s_waitcnt vmcnt(3)
	v_mov_b32_e32 v2, 0x3e020821
	v_cmp_gt_u32_e64 s[0:1], 32, v1
	v_mov_b32_e32 v68, 0xffff
	v_cmp_ne_u32_e32 vcc, 0, v54
	v_cndmask_b32_e64 v67, v2, 0, s[0:1]
	s_waitcnt vmcnt(0)
	v_lshrrev_b32_e32 v2, 16, v55
	v_lshrrev_b32_e32 v0, 1, v0
	v_mov_b32_e32 v3, 0x7a00
	v_ashrrev_i32_e32 v65, 31, v64
	v_lshlrev_b32_e32 v52, 2, v1
	v_cndmask_b32_e32 v95, v68, v2, vcc
	s_lshl_b32 s12, s10, 2
	v_lshlrev_b32_e32 v2, 4, v1
	v_and_or_b32 v70, v0, 16, v3
	v_lshlrev_b32_e32 v73, 1, v1
	v_lshlrev_b64 v[0:1], 8, v[64:65]
	v_mov_b32_e32 v53, 0
	v_or_b32_e32 v0, v0, v52
	s_ashr_i32 s13, s12, 31
	s_mov_b32 s11, 0
	v_add_u32_e32 v69, 0x3200, v2
	v_add_u32_e32 v71, 0x5200, v2
	v_add_u32_e32 v72, 0x7200, v2
	s_waitcnt lgkmcnt(0)
	v_lshl_add_u64 v[60:61], s[6:7], 0, v[52:53]
	v_lshl_add_u64 v[62:63], s[2:3], 0, v[0:1]
	s_lshl_b64 s[6:7], s[12:13], 8
	s_mov_b64 s[14:15], 0
	s_movk_i32 s13, 0x61a7
	v_mov_b32_e32 v65, 0xc0669d92
	s_mov_b32 s22, 0xc1c00000
	v_mov_b32_e32 v74, 0x41c00000
	v_mov_b32_e32 v75, 0xbfb8aa3b
	v_mov_b32_e32 v76, 0xc1b69213
	v_mov_b32_e32 v77, 0xc228283a
	v_mov_b32_e32 v78, 0xc275076b
	s_mov_b32 s16, 0x3e0a9555
	v_mov_b32_e32 v79, v52
	s_mov_b32 s94, 0
	s_branch .LBB4_11
.LBB4_10:
	s_and_b64 s[2:3], exec, s[2:3]
	s_or_b64 s[14:15], s[2:3], s[14:15]
	v_readlane_b32 s2, v50, 31
	s_bfe_u32 s3, s2, 0x80008
	v_lshl_or_b32 v0, s3, 7, v73
	ds_read_u16 v0, v0
	s_bfe_u32 s2, s2, 0x100010
	s_lshl_b32 s10, s2, 8
	v_fma_mix_f32 v32, v15, v81, v32 op_sel:[0,1,0] op_sel_hi:[0,1,0]
	v_fma_mix_f32 v33, v15, v81, v33 op_sel_hi:[0,1,0]
	s_nop 0
	v_cndmask_b32_sdwa v95, v51, v68, vcc dst_sel:DWORD dst_unused:UNUSED_PAD src0_sel:WORD_1 src1_sel:DWORD
	s_waitcnt lgkmcnt(0)
	v_fma_mix_f32 v2, v0, v33, v32 op_sel_hi:[1,0,0]
	v_lshl_add_u64 v[0:1], v[60:61], 0, s[10:11]
	v_cndmask_b32_e64 v1, v63, v1, s[20:21]
	v_cndmask_b32_e64 v0, v62, v0, s[20:21]
	v_lshl_add_u64 v[62:63], v[62:63], 0, s[6:7]
	v_mov_b64_e32 v[48:49], v[56:57]
	v_mov_b64_e32 v[50:51], v[58:59]
	global_store_dword v[0:1], v2, off sc1
	s_andn2_b64 exec, exec, s[14:15]
	s_cbranch_execz .LBB4_73

.Lprio_e1_done:
	s_add_u32 s94, s94, 1
	v_sub_f32_e32 v39, v48, v67
	v_fmamk_f32 v32, v39, 0x4297576a, v65
	v_fmamk_f32 v33, v39, 0x4297576a, v76
	v_med3_f32 v35, v32, s22, v74
	v_med3_f32 v37, v33, s22, v74
	v_mul_f32_e64 v32, v35, -v35
	v_fmamk_f32 v34, v35, 0x4019be61, v75
	v_mul_f32_e64 v33, v37, -v37
	v_fmamk_f32 v35, v35, 0xc019be61, v75
	v_exp_f32_e32 v32, v32
	v_exp_f32_e32 v33, v33
	v_exp_f32_e32 v36, v35
	v_fmamk_f32 v35, v37, 0x4019be61, v75
	v_exp_f32_e32 v34, v34
	v_exp_f32_e32 v35, v35
	v_fmamk_f32 v37, v37, 0xc019be61, v75
	v_exp_f32_e32 v37, v37
	v_pk_mul_f32 v[32:33], v[48:49], v[32:33] op_sel:[1,0]
	ds_read_b128 v[28:31], v69
	ds_read_b128 v[24:27], v69 offset:1024
	ds_read_b128 v[20:23], v69 offset:2048
	ds_read_b128 v[16:19], v69 offset:3072
	ds_read_b128 v[0:3], v70
	ds_read_b128 v[4:7], v70 offset:32
	ds_read_b128 v[8:11], v70 offset:64
	ds_read_b128 v[12:15], v70 offset:96
	v_pk_mul_f32 v[44:45], v[34:35], v[32:33]
	v_pk_mul_f32 v[34:35], v[34:35], s[16:17] op_sel_hi:[1,0]
	v_mov_b32_e32 v99, v80
	v_fmamk_f32 v38, v39, 0x4297576a, v77
	v_fmamk_f32 v39, v39, 0x4297576a, v78
	v_pk_mul_f32 v[46:47], v[34:35], v[44:45]
	v_pk_mul_f32 v[34:35], v[34:35], s[16:17] op_sel_hi:[1,0]
	v_pk_mul_f32 v[80:81], v[36:37], v[32:33]
	v_pk_mul_f32 v[36:37], v[36:37], s[16:17] op_sel_hi:[1,0]
	v_med3_f32 v41, v38, s22, v74
	v_med3_f32 v43, v39, s22, v74
	v_pk_mul_f32 v[58:59], v[34:35], v[46:47]
	v_pk_mul_f32 v[34:35], v[34:35], s[16:17] op_sel_hi:[1,0]
	v_pk_mul_f32 v[82:83], v[36:37], v[80:81]
	v_pk_mul_f32 v[36:37], v[36:37], s[16:17] op_sel_hi:[1,0]
	v_mul_f32_e64 v38, v41, -v41
	v_fmamk_f32 v40, v41, 0x4019be61, v75
	v_mul_f32_e64 v39, v43, -v43
	v_fmamk_f32 v41, v41, 0xc019be61, v75
	v_pk_mul_f32 v[34:35], v[34:35], v[58:59]
	v_pk_mul_f32 v[36:37], v[36:37], v[82:83]
	v_exp_f32_e32 v38, v38
	v_exp_f32_e32 v39, v39
	v_exp_f32_e32 v42, v41
	v_fmamk_f32 v41, v43, 0x4019be61, v75
	v_cvt_pk_f16_f32 v56, v44, v46
	v_cvt_pk_f16_f32 v54, v36, v82
	v_cvt_pk_f16_f32 v57, v58, v34
	v_cvt_pk_f16_f32 v55, v80, v32
	v_exp_f32_e32 v40, v40
	v_exp_f32_e32 v41, v41
	s_waitcnt lgkmcnt(0)
	v_mfma_f32_32x32x16_f16 v[0:15], v[28:31], v[54:57], v[0:15]
	v_mul_f32_e64 v38, v49, v38
	v_mul_f32_e64 v39, v49, v39
	v_fmamk_f32 v43, v43, 0xc019be61, v75
	v_mul_f32_e64 v84, v40, v38
	v_mul_f32_e64 v85, v41, v39
	v_pk_mul_f32 v[40:41], v[40:41], s[16:17] op_sel_hi:[1,0]
	v_cvt_pk_f16_f32 v30, v45, v47
	v_pk_mul_f32 v[86:87], v[40:41], v[84:85]
	v_pk_mul_f32 v[28:29], v[40:41], s[16:17] op_sel_hi:[1,0]
	v_cvt_pk_f16_f32 v31, v59, v35
	v_pk_mul_f32 v[40:41], v[28:29], v[86:87]
	v_pk_mul_f32 v[28:29], v[28:29], s[16:17] op_sel_hi:[1,0]
	v_exp_f32_e32 v43, v43
	v_pk_mul_f32 v[88:89], v[28:29], v[40:41]
	v_cvt_pk_f16_f32 v28, v37, v83
	v_cvt_pk_f16_f32 v29, v81, v33
	v_pk_mul_f32 v[36:37], v[42:43], v[38:39]
	v_pk_mul_f32 v[42:43], v[42:43], s[16:17] op_sel_hi:[1,0]
	v_mfma_f32_32x32x16_f16 v[0:15], v[24:27], v[28:31], v[0:15]
	v_mul_f32_e64 v32, v42, v36
	v_mul_f32_e64 v33, v43, v37
	v_mul_f32_e64 v24, v42, s16
	v_mul_f32_e64 v25, v43, s16
	v_cvt_pk_f16_f32 v26, v84, v86
	v_pk_mul_f32 v[34:35], v[24:25], v[32:33]
	v_cvt_pk_f16_f32 v27, v40, v88
	v_cvt_pk_f16_f32 v24, v34, v32
	v_cvt_pk_f16_f32 v25, v36, v38
	v_cvt_pk_f16_f32 v84, v85, v87
	v_cvt_pk_f16_f32 v82, v35, v33
	v_mfma_f32_32x32x16_f16 v[0:15], v[20:23], v[24:27], v[0:15]
	ds_read_b128 v[20:23], v69 offset:4096
	v_cvt_pk_f16_f32 v85, v41, v89
	v_cvt_pk_f16_f32 v83, v37, v39
	ds_read_b128 v[32:35], v70 offset:128
	ds_read_b128 v[36:39], v70 offset:160
	ds_read_b128 v[40:43], v70 offset:192
	ds_read_b128 v[44:47], v70 offset:224
	v_mov_b32_e32 v52, v64
	v_add_u32_e32 v64, s12, v52
	v_readlane_b32 s48, v51, 0
	v_mfma_f32_32x32x16_f16 v[0:15], v[16:19], v[82:85], v[0:15]
	ds_read_b128 v[16:19], v69 offset:5120
	v_cmp_gt_i32_e32 vcc, s17, v64
	s_lshl_b32 s48, s48, 8
	s_and_b32 s48, s48, 0xffff00
	v_readlane_b32 s47, v51, 1
	s_add_u32 s48, s4, s48
	s_addc_u32 s49, s5, 0
	s_waitcnt lgkmcnt(1)
	v_mfma_f32_32x32x16_f16 v[32:47], v[20:23], v[54:57], v[32:47]
	ds_read_b128 v[20:23], v69 offset:6144
	s_lshl_b32 s47, s47, 8
	s_and_b32 s47, s47, 0xffff00
	v_readlane_b32 s46, v51, 2
	v_readlane_b32 s45, v51, 3
	v_readlane_b32 s44, v51, 4
	v_readlane_b32 s43, v51, 5
	s_waitcnt lgkmcnt(1)
	v_mfma_f32_32x32x16_f16 v[32:47], v[16:19], v[28:31], v[32:47]
	v_cndmask_b32_e32 v16, v52, v64, vcc
	v_lshl_or_b32 v28, v16, 5, v66
	v_cmp_eq_u32_e32 vcc, 0, v28
	v_ashrrev_i32_e32 v29, 31, v28
	v_lshl_add_u64 v[30:31], v[28:29], 4, s[8:9]
	v_readlane_b32 s3, v51, 6
	v_readlane_b32 s2, v51, 7
	s_waitcnt lgkmcnt(0)
	v_mfma_f32_32x32x16_f16 v[32:47], v[20:23], v[24:27], v[32:47]
	v_cndmask_b32_e64 v20, 0, 1, vcc
	v_lshlrev_b32_e32 v52, 4, v20
	v_readlane_b32 s36, v51, 8
	v_readlane_b32 s35, v51, 9
	v_readlane_b32 s34, v51, 10
	v_readlane_b32 s33, v51, 11
	v_readlane_b32 s31, v51, 12
	v_readlane_b32 s30, v51, 13
	v_readlane_b32 s29, v51, 14
	v_readlane_b32 s28, v51, 15
	v_readlane_b32 s27, v51, 16
	v_readlane_b32 s26, v51, 17
	v_readlane_b32 s25, v51, 18
	v_readlane_b32 s24, v51, 19
	v_readlane_b32 s23, v51, 20
	v_readlane_b32 s42, v51, 21
	v_readlane_b32 s41, v51, 22
	v_readlane_b32 s40, v51, 23
	v_readlane_b32 s39, v51, 24
	v_readlane_b32 s38, v51, 25
	v_readlane_b32 s37, v51, 26
	v_readlane_b32 s21, v51, 27
	v_readlane_b32 s20, v51, 28
	v_readlane_b32 s19, v51, 29
	v_readlane_b32 s18, v51, 30
	v_readlane_b32 s10, v51, 31
	ds_read_b128 v[16:19], v69 offset:7168
	v_lshl_add_u64 v[20:21], v[30:31], 0, v[52:53]
	global_load_dwordx4 v[56:59], v[30:31], off
	global_load_dword v80, v[30:31], off offset:24
	global_load_dword v51, v[20:21], off offset:-8
	global_load_dword v112, v79, s[48:49]
	s_add_u32 s48, s4, s47
	s_addc_u32 s49, s5, 0
	s_lshl_b32 s46, s46, 8
	s_and_b32 s46, s46, 0xffff00
	s_add_u32 s46, s4, s46
	s_addc_u32 s47, s5, 0
	s_lshl_b32 s45, s45, 8
	s_and_b32 s45, s45, 0xffff00
	global_load_dword v110, v79, s[48:49]
	global_load_dword v108, v79, s[46:47]
	s_add_u32 s46, s4, s45
	s_addc_u32 s47, s5, 0
	s_lshl_b32 s44, s44, 8
	s_and_b32 s44, s44, 0xffff00
	s_add_u32 s44, s4, s44
	s_addc_u32 s45, s5, 0
	s_lshl_b32 s43, s43, 8
	s_and_b32 s43, s43, 0xffff00
	global_load_dword v106, v79, s[46:47]
	global_load_dword v104, v79, s[44:45]
	s_add_u32 s44, s4, s43
	s_addc_u32 s45, s5, 0
	s_lshl_b32 s3, s3, 8
	s_and_b32 s3, s3, 0xffff00
	global_load_dword v102, v79, s[44:45]
	s_add_u32 s44, s4, s3
	s_addc_u32 s45, s5, 0
	s_lshl_b32 s2, s2, 8
	s_and_b32 s2, s2, 0xffff00
	s_add_u32 s2, s4, s2
	global_load_dword v100, v79, s[44:45]
	s_addc_u32 s3, s5, 0
	global_load_dword v114, v79, s[2:3]
	s_lshl_b32 s2, s36, 8
	s_and_b32 s2, s2, 0xffff00
	s_add_u32 s2, s4, s2
	s_addc_u32 s3, s5, 0
	global_load_dword v113, v79, s[2:3]
	s_lshl_b32 s2, s35, 8
	s_and_b32 s2, s2, 0xffff00
	s_add_u32 s2, s4, s2
	s_addc_u32 s3, s5, 0
	global_load_dword v111, v79, s[2:3]
	s_lshl_b32 s2, s34, 8
	s_and_b32 s2, s2, 0xffff00
	s_add_u32 s2, s4, s2
	s_addc_u32 s3, s5, 0
	global_load_dword v109, v79, s[2:3]
	s_lshl_b32 s2, s33, 8
	s_and_b32 s2, s2, 0xffff00
	s_add_u32 s2, s4, s2
	s_addc_u32 s3, s5, 0
	global_load_dword v107, v79, s[2:3]
	s_lshl_b32 s2, s31, 8
	s_and_b32 s2, s2, 0xffff00
	s_add_u32 s2, s4, s2
	s_addc_u32 s3, s5, 0
	global_load_dword v105, v79, s[2:3]
	s_lshl_b32 s2, s30, 8
	s_and_b32 s2, s2, 0xffff00
	s_add_u32 s2, s4, s2
	s_addc_u32 s3, s5, 0
	global_load_dword v103, v79, s[2:3]
	s_lshl_b32 s2, s29, 8
	s_and_b32 s2, s2, 0xffff00
	s_add_u32 s2, s4, s2
	s_addc_u32 s3, s5, 0
	global_load_dword v101, v79, s[2:3]
	s_lshl_b32 s2, s28, 8
	s_and_b32 s2, s2, 0xffff00
	s_add_u32 s2, s4, s2
	s_addc_u32 s3, s5, 0
	global_load_dword v98, v79, s[2:3]
	s_lshl_b32 s2, s27, 8
	s_and_b32 s2, s2, 0xffff00
	s_add_u32 s2, s4, s2
	s_addc_u32 s3, s5, 0
	global_load_dword v97, v79, s[2:3]
	s_lshl_b32 s2, s26, 8
	s_and_b32 s2, s2, 0xffff00
	s_add_u32 s2, s4, s2
	s_addc_u32 s3, s5, 0
	global_load_dword v96, v79, s[2:3]
	s_lshl_b32 s2, s25, 8
	s_and_b32 s2, s2, 0xffff00
	s_add_u32 s2, s4, s2
	s_addc_u32 s3, s5, 0
	global_load_dword v94, v79, s[2:3]
	s_lshl_b32 s2, s24, 8
	s_and_b32 s2, s2, 0xffff00
	s_add_u32 s2, s4, s2
	s_addc_u32 s3, s5, 0
	global_load_dword v91, v79, s[2:3]
	s_lshl_b32 s2, s23, 8
	s_and_b32 s2, s2, 0xffff00
	s_add_u32 s2, s4, s2
	s_addc_u32 s3, s5, 0
	global_load_dword v93, v79, s[2:3]
	s_lshl_b32 s2, s42, 8
	s_and_b32 s2, s2, 0xffff00
	s_add_u32 s2, s4, s2
	s_addc_u32 s3, s5, 0
	global_load_dword v90, v79, s[2:3]
	s_lshl_b32 s2, s41, 8
	s_and_b32 s2, s2, 0xffff00
	s_add_u32 s2, s4, s2
	s_addc_u32 s3, s5, 0
	global_load_dword v88, v79, s[2:3]
	s_lshl_b32 s2, s40, 8
	s_and_b32 s2, s2, 0xffff00
	s_add_u32 s2, s4, s2
	s_addc_u32 s3, s5, 0
	global_load_dword v86, v79, s[2:3]
	s_lshl_b32 s2, s39, 8
	s_and_b32 s2, s2, 0xffff00
	v_min_f32 v0, 0x42fc0000, v0
	v_min_f32 v1, 0x42fc0000, v1
	s_add_u32 s2, s4, s2
	s_waitcnt lgkmcnt(0)
	v_mfma_f32_32x32x16_f16 v[32:47], v[16:19], v[82:85], v[32:47]
	v_exp_f32_e32 v0, v0
	v_exp_f32_e32 v1, v1
	s_addc_u32 s3, s5, 0
	global_load_dword v85, v79, s[2:3]
	s_lshl_b32 s2, s38, 8
	s_and_b32 s2, s2, 0xffff00
	v_min_f32 v6, 0x42fc0000, v6
	v_min_f32 v7, 0x42fc0000, v7
	s_add_u32 s2, s4, s2
	v_exp_f32_e32 v6, v6
	v_exp_f32_e32 v7, v7
	s_addc_u32 s3, s5, 0
	global_load_dword v83, v79, s[2:3]
	s_lshl_b32 s2, s37, 8
	v_pk_add_f32 v[0:1], v[0:1], 1.0 op_sel_hi:[1,0]
	s_and_b32 s2, s2, 0xffff00
	v_min_f32 v2, 0x42fc0000, v2
	v_min_f32 v3, 0x42fc0000, v3
	v_min_f32 v16, 0x42fc0000, v4
	v_min_f32 v17, 0x42fc0000, v5
	v_log_f32_e32 v4, v0
	v_log_f32_e32 v5, v1
	v_exp_f32_e32 v0, v16
	v_exp_f32_e32 v1, v17
	s_add_u32 s2, s4, s2
	v_exp_f32_e32 v2, v2
	v_exp_f32_e32 v3, v3
	s_addc_u32 s3, s5, 0
	global_load_dword v92, v79, s[2:3]
	s_lshl_b32 s2, s21, 8
	v_pk_add_f32 v[6:7], v[6:7], 1.0 op_sel_hi:[1,0]
	s_and_b32 s2, s2, 0xffff00
	v_log_f32_e32 v6, v6
	v_log_f32_e32 v7, v7
	s_add_u32 s2, s4, s2
	v_pk_add_f32 v[0:1], v[0:1], 1.0 op_sel_hi:[1,0]
	s_addc_u32 s3, s5, 0
	global_load_dword v89, v79, s[2:3]
	s_lshl_b32 s2, s20, 8
	v_pk_add_f32 v[2:3], v[2:3], 1.0 op_sel_hi:[1,0]
	v_log_f32_e32 v0, v0
	v_log_f32_e32 v1, v1
	s_and_b32 s2, s2, 0xffff00
	v_min_f32 v18, 0x42fc0000, v8
	v_min_f32 v19, 0x42fc0000, v9
	v_log_f32_e32 v8, v2
	v_log_f32_e32 v9, v3
	s_add_u32 s2, s4, s2
	v_pk_mul_f32 v[2:3], v[48:49], v[6:7] op_sel:[1,0]
	v_exp_f32_e32 v6, v18
	v_exp_f32_e32 v7, v19
	s_addc_u32 s3, s5, 0
	s_lshl_b32 s19, s19, 8
	s_and_b32 s19, s19, 0xffff00
	v_pk_mul_f32 v[0:1], v[48:49], v[0:1] op_sel:[1,0]
	s_add_u32 s20, s4, s19
	v_min_f32 v10, 0x42fc0000, v10
	v_min_f32 v11, 0x42fc0000, v11
	v_cvt_pk_f16_f32 v3, v2, v3
	v_cvt_pk_f16_f32 v2, v0, v1
	v_pk_mul_f32 v[0:1], v[48:49], v[8:9] op_sel:[1,0]
	v_pk_mul_f32 v[4:5], v[48:49], v[4:5] op_sel:[1,0]
	s_addc_u32 s21, s5, 0
	s_lshl_b32 s18, s18, 8
	v_min_f32 v12, 0x42fc0000, v12
	v_min_f32 v13, 0x42fc0000, v13
	v_min_f32 v14, 0x42fc0000, v14
	v_min_f32 v15, 0x42fc0000, v15
	v_cvt_pk_f16_f32 v1, v0, v1
	v_cvt_pk_f16_f32 v0, v4, v5
	v_pk_add_f32 v[4:5], v[6:7], 1.0 op_sel_hi:[1,0]
	v_exp_f32_e32 v6, v10
	v_exp_f32_e32 v7, v11
	v_exp_f32_e32 v8, v12
	v_exp_f32_e32 v9, v13
	v_exp_f32_e32 v10, v14
	v_exp_f32_e32 v11, v15
	s_and_b32 s18, s18, 0xffff00
	s_add_u32 s18, s4, s18
	s_addc_u32 s19, s5, 0
	s_lshl_b32 s10, s10, 8
	s_and_b32 s10, s10, 0xffff00
	v_pk_add_f32 v[8:9], v[8:9], 1.0 op_sel_hi:[1,0]
	v_pk_add_f32 v[10:11], v[10:11], 1.0 op_sel_hi:[1,0]
	s_add_u32 s24, s4, s10
	v_pk_add_f32 v[6:7], v[6:7], 1.0 op_sel_hi:[1,0]
	v_log_f32_e32 v8, v8
	v_log_f32_e32 v9, v9
	v_log_f32_e32 v10, v10
	v_log_f32_e32 v11, v11
	s_addc_u32 s25, s5, 0
	global_load_dword v87, v79, s[2:3]
	global_load_dword v84, v79, s[20:21]
	global_load_dword v82, v79, s[18:19]
	global_load_dword v81, v79, s[24:25]
	ds_read_b128 v[12:15], v71
	v_log_f32_e32 v6, v6
	v_log_f32_e32 v7, v7
	v_log_f32_e32 v4, v4
	v_log_f32_e32 v5, v5
	v_pk_mul_f32 v[8:9], v[48:49], v[8:9] op_sel:[1,0]
	v_pk_mul_f32 v[10:11], v[48:49], v[10:11] op_sel:[1,0]
	v_cvt_pk_f16_f32 v118, v8, v9
	v_cvt_pk_f16_f32 v119, v10, v11
	v_pk_mul_f32 v[10:11], v[48:49], v[6:7] op_sel:[1,0]
	ds_read_b128 v[6:9], v71 offset:1024
	s_waitcnt lgkmcnt(1)
	v_mfma_f32_32x32x16_f16 v[16:31], v[0:3], v[12:15], 0
	v_min_f32 v32, 0x42fc0000, v32
	v_min_f32 v33, 0x42fc0000, v33
	v_mul_f32_e64 v4, v49, v4
	v_mul_f32_e64 v5, v49, v5
	v_exp_f32_e32 v32, v32
	v_exp_f32_e32 v33, v33
	v_min_f32 v36, 0x42fc0000, v36
	v_min_f32 v37, 0x42fc0000, v37
	v_cvt_pk_f16_f32 v117, v10, v11
	v_cvt_pk_f16_f32 v116, v4, v5
	v_exp_f32_e32 v36, v36
	v_exp_f32_e32 v37, v37
	v_pk_add_f32 v[32:33], v[32:33], 1.0 op_sel_hi:[1,0]
	s_waitcnt lgkmcnt(0)
	v_mfma_f32_32x32x16_f16 v[16:31], v[116:119], v[6:9], v[16:31]
	v_log_f32_e32 v54, v32
	v_log_f32_e32 v55, v33
	v_pk_add_f32 v[32:33], v[36:37], 1.0 op_sel_hi:[1,0]
	v_min_f32 v36, 0x42fc0000, v38
	v_min_f32 v37, 0x42fc0000, v39
	ds_read_b128 v[4:7], v71 offset:4096
	ds_read_b128 v[120:123], v71 offset:5120
	v_exp_f32_e32 v36, v36
	v_exp_f32_e32 v37, v37
	v_min_f32 v34, 0x42fc0000, v34
	v_min_f32 v35, 0x42fc0000, v35
	s_waitcnt lgkmcnt(1)
	v_mfma_f32_32x32x16_f16 v[0:15], v[0:3], v[4:7], 0
	v_exp_f32_e32 v34, v34
	v_exp_f32_e32 v35, v35
	v_pk_add_f32 v[36:37], v[36:37], 1.0 op_sel_hi:[1,0]
	v_log_f32_e32 v32, v32
	v_log_f32_e32 v33, v33
	v_log_f32_e32 v36, v36
	v_log_f32_e32 v37, v37
	v_pk_add_f32 v[34:35], v[34:35], 1.0 op_sel_hi:[1,0]
	v_pk_mul_f32 v[32:33], v[48:49], v[32:33] op_sel:[1,0]
	v_log_f32_e32 v38, v34
	v_log_f32_e32 v39, v35
	v_pk_mul_f32 v[34:35], v[48:49], v[36:37] op_sel:[1,0]
	v_pk_mul_f32 v[36:37], v[48:49], v[54:55] op_sel:[1,0]
	v_cvt_pk_f16_f32 v35, v34, v35
	v_cvt_pk_f16_f32 v34, v32, v33
	v_pk_mul_f32 v[32:33], v[48:49], v[38:39] op_sel:[1,0]
	s_waitcnt lgkmcnt(0)
	v_mfma_f32_32x32x16_f16 v[0:15], v[116:119], v[120:123], v[0:15]
	v_cvt_pk_f16_f32 v33, v32, v33
	v_cvt_pk_f16_f32 v32, v36, v37
	ds_read_b128 v[36:39], v71 offset:2048
	ds_read_b128 v[116:119], v71 offset:3072
	v_min_f32 v40, 0x42fc0000, v40
	v_min_f32 v41, 0x42fc0000, v41
	v_min_f32 v55, 0x42fc0000, v44
	v_min_f32 v115, 0x42fc0000, v45
	s_waitcnt lgkmcnt(1)
	v_mfma_f32_32x32x16_f16 v[16:31], v[32:35], v[36:39], v[16:31]
	ds_read_b128 v[36:39], v71 offset:6144
	v_exp_f32_e32 v44, v40
	v_exp_f32_e32 v45, v41
	v_min_f32 v52, 0x42fc0000, v42
	v_min_f32 v54, 0x42fc0000, v43
	ds_read_b128 v[40:43], v71 offset:7168
	v_min_f32 v46, 0x42fc0000, v46
	s_waitcnt lgkmcnt(1)
	v_mfma_f32_32x32x16_f16 v[0:15], v[32:35], v[36:39], v[0:15]
	v_add_f32_e64 v34, v44, 1.0
	v_add_f32_e64 v35, v45, 1.0
	v_min_f32 v47, 0x42fc0000, v47
	v_exp_f32_e32 v32, v55
	v_exp_f32_e32 v33, v115
	v_log_f32_e32 v36, v34
	v_log_f32_e32 v37, v35
	v_exp_f32_e32 v34, v46
	v_exp_f32_e32 v35, v47
	v_exp_f32_e32 v38, v52
	v_exp_f32_e32 v39, v54
	v_pk_add_f32 v[32:33], v[32:33], 1.0 op_sel_hi:[1,0]
	v_pk_add_f32 v[34:35], v[34:35], 1.0 op_sel_hi:[1,0]
	v_log_f32_e32 v32, v32
	v_log_f32_e32 v33, v33
	v_log_f32_e32 v34, v34
	v_log_f32_e32 v35, v35
	v_pk_add_f32 v[38:39], v[38:39], 1.0 op_sel_hi:[1,0]
	v_pk_mul_f32 v[32:33], v[48:49], v[32:33] op_sel:[1,0]
	v_log_f32_e32 v38, v38
	v_log_f32_e32 v39, v39
	v_pk_mul_f32 v[34:35], v[48:49], v[34:35] op_sel:[1,0]
	v_pk_mul_f32 v[36:37], v[48:49], v[36:37] op_sel:[1,0]
	v_cvt_pk_f16_f32 v35, v34, v35
	v_cvt_pk_f16_f32 v34, v32, v33
	v_pk_mul_f32 v[32:33], v[48:49], v[38:39] op_sel:[1,0]
	v_mov_b32_e32 v54, v53
	v_cvt_pk_f16_f32 v33, v32, v33
	v_cvt_pk_f16_f32 v32, v36, v37
	v_cvt_f16_f32_e32 v36, v49
	v_mov_b32_e32 v55, v53
	v_mfma_f32_32x32x16_f16 v[16:31], v[32:35], v[116:119], v[16:31]
	v_cmp_ne_u32_sdwa s[20:21], v95, v50 src0_sel:DWORD src1_sel:WORD_1
	v_cmp_ne_u32_sdwa s[18:19], v99, v50 src0_sel:WORD_1 src1_sel:WORD_1
	s_bitcmp1_b32 s20, 0
	v_cmp_lt_i32_e64 s[2:3], s13, v64
	s_cselect_b64 s[20:21], -1, 0
	s_bitcmp0_b32 s18, 0
	s_waitcnt lgkmcnt(0)
	v_mfma_f32_32x32x16_f16 v[0:15], v[32:35], v[40:43], v[0:15]
	v_cndmask_b32_e64 v32, 0, v36, s[0:1]
	v_pack_b32_f16 v52, v32, 0
	ds_read_b128 v[32:35], v72
	ds_read_b128 v[36:39], v72 offset:1024
	s_waitcnt vmcnt(0)
	s_waitcnt vmcnt(0)
	s_waitcnt lgkmcnt(1)
	v_mfma_f32_32x32x16_f16 v[16:31], v[52:55], v[32:35], v[16:31]
	v_mov_b32_e32 v32, 0
	v_mov_b32_e32 v33, 0
	s_waitcnt lgkmcnt(0)
	v_mfma_f32_32x32x16_f16 v[0:15], v[52:55], v[36:39], v[0:15]
	s_nop 11
	v_permlane32_swap_b32_e32 v16, v0
	v_permlane32_swap_b32_e32 v17, v1
	v_permlane32_swap_b32_e32 v18, v2
	v_permlane32_swap_b32_e32 v19, v3
	v_permlane32_swap_b32_e32 v20, v4
	v_permlane32_swap_b32_e32 v21, v5
	v_permlane32_swap_b32_e32 v22, v6
	v_permlane32_swap_b32_e32 v23, v7
	v_permlane32_swap_b32_e32 v24, v8
	v_permlane32_swap_b32_e32 v25, v9
	v_permlane32_swap_b32_e32 v26, v10
	v_permlane32_swap_b32_e32 v27, v11
	v_permlane32_swap_b32_e32 v28, v12
	v_permlane32_swap_b32_e32 v29, v13
	v_permlane32_swap_b32_e32 v30, v14
	v_permlane32_swap_b32_e32 v31, v15
	v_fma_mix_f32 v32, v16, v112, v32 op_sel:[0,1,0] op_sel_hi:[0,1,0]
	v_fma_mix_f32 v33, v16, v112, v33 op_sel_hi:[0,1,0]
	s_cbranch_scc1 .LBB4_13
	v_readlane_b32 s10, v50, 0
	s_bfe_u32 s19, s10, 0x80008
	v_lshl_or_b32 v16, s19, 7, v73
	ds_read_u16 v16, v16
	s_bfe_u32 s10, s10, 0x100010
	s_lshl_b32 s10, s10, 8
	v_lshl_add_u64 v[34:35], v[60:61], 0, s[10:11]
	v_cndmask_b32_e64 v35, v63, v35, s[20:21]
	s_waitcnt lgkmcnt(0)
	v_fma_mix_f32 v16, v16, v33, v32 op_sel_hi:[1,0,0]
	v_cndmask_b32_e64 v34, v62, v34, s[20:21]
	s_mov_b64 s[20:21], -1
	v_mov_b32_e32 v32, 0
	v_mov_b32_e32 v33, 0
	global_store_dword v[34:35], v16, off sc1

_Z7k_finalPKfS0_S0_S0_S0_S0_Pf:
	s_load_dwordx8 s[4:11], s[0:1], 0x0
	s_load_dwordx4 s[12:15], s[0:1], 0x20
	s_load_dwordx2 s[16:17], s[0:1], 0x30
	v_lshlrev_b32_e32 v2, 2, v0
	v_lshlrev_b32_e32 v3, 4, v0
	v_min_u32_e32 v7, 9, v0
	s_lshl_b32 s18, s2, 2
	s_lshl_b32 s19, s2, 8
	v_lshlrev_b32_e32 v7, 2, v7
	s_waitcnt lgkmcnt(0)
	s_add_u32 s6, s6, s18
	s_addc_u32 s7, s7, 0
	s_load_dword s3, s[6:7], 0x0
	s_add_u32 s4, s4, s19
	s_addc_u32 s5, s5, 0
	s_add_u32 s20, s8, 0x1000
	s_addc_u32 s21, s9, 0
	s_add_u32 s22, s8, 0x2000
	s_addc_u32 s23, s9, 0
	s_add_u32 s24, s8, 0x3000
	s_addc_u32 s25, s9, 0
	global_load_dword v1, v2, s[4:5]
	global_load_dword v4, v2, s[10:11]
	global_load_dwordx4 v[8:11], v3, s[8:9]
	global_load_dwordx4 v[12:15], v3, s[8:9] offset:1024
	global_load_dwordx4 v[16:19], v3, s[8:9] offset:2048
	global_load_dwordx4 v[20:23], v3, s[8:9] offset:3072
	global_load_dwordx4 v[24:27], v3, s[20:21]
	global_load_dwordx4 v[28:31], v3, s[20:21] offset:1024
	global_load_dwordx4 v[32:35], v3, s[20:21] offset:2048
	global_load_dwordx4 v[36:39], v3, s[20:21] offset:3072
	global_load_dwordx4 v[40:43], v3, s[22:23]
	global_load_dwordx4 v[44:47], v3, s[22:23] offset:1024
	global_load_dwordx4 v[48:51], v3, s[22:23] offset:2048
	global_load_dwordx4 v[52:55], v3, s[22:23] offset:3072
	global_load_dwordx4 v[56:59], v3, s[24:25]
	global_load_dwordx4 v[60:63], v3, s[24:25] offset:1024
	global_load_dwordx4 v[64:67], v3, s[24:25] offset:2048
	global_load_dwordx4 v[68:71], v3, s[24:25] offset:3072
	global_load_dword v72, v2, s[12:13]
	global_load_dword v73, v2, s[12:13] offset:256
	global_load_dword v74, v2, s[12:13] offset:512
	global_load_dword v75, v2, s[12:13] offset:768
	global_load_dword v76, v2, s[12:13] offset:1024
	global_load_dword v77, v2, s[12:13] offset:1280
	global_load_dword v78, v2, s[12:13] offset:1536
	global_load_dword v79, v2, s[12:13] offset:1792
	global_load_dword v80, v2, s[12:13] offset:2048
	global_load_dword v81, v2, s[12:13] offset:2304
	global_load_dword v5, v7, s[14:15]
	s_mul_i32 s18, s2, 40
	s_waitcnt vmcnt(11)
	ds_write_b128 v3, v[8:11]
	ds_write_b128 v3, v[12:15] offset:1024
	ds_write_b128 v3, v[16:19] offset:2048
	ds_write_b128 v3, v[20:23] offset:3072
	ds_write_b128 v3, v[24:27] offset:4096
	ds_write_b128 v3, v[28:31] offset:5120
	ds_write_b128 v3, v[32:35] offset:6144
	ds_write_b128 v3, v[36:39] offset:7168
	ds_write_b128 v3, v[40:43] offset:8192
	ds_write_b128 v3, v[44:47] offset:9216
	ds_write_b128 v3, v[48:51] offset:10240
	ds_write_b128 v3, v[52:55] offset:11264
	ds_write_b128 v3, v[56:59] offset:12288
	ds_write_b128 v3, v[60:63] offset:13312
	ds_write_b128 v3, v[64:67] offset:14336
	ds_write_b128 v3, v[68:71] offset:15360
	s_waitcnt vmcnt(1)
	ds_write_b32 v2, v72 offset:16384
	ds_write_b32 v2, v73 offset:16640
	ds_write_b32 v2, v74 offset:16896
	ds_write_b32 v2, v75 offset:17152
	ds_write_b32 v2, v76 offset:17408
	ds_write_b32 v2, v77 offset:17664
	ds_write_b32 v2, v78 offset:17920
	ds_write_b32 v2, v79 offset:18176
	ds_write_b32 v2, v80 offset:18432
	ds_write_b32 v2, v81 offset:18688
	ds_read_b32 v80, v2
	ds_read_b32 v81, v2 offset:256
	ds_read_b32 v82, v2 offset:512
	ds_read_b32 v83, v2 offset:768
	ds_read_b32 v84, v2 offset:1024
	ds_read_b32 v85, v2 offset:1280
	ds_read_b32 v86, v2 offset:1536
	ds_read_b32 v87, v2 offset:1792
	ds_read_b32 v88, v2 offset:2048
	ds_read_b32 v89, v2 offset:2304
	ds_read_b32 v90, v2 offset:2560
	ds_read_b32 v91, v2 offset:2816
	ds_read_b32 v92, v2 offset:3072
	ds_read_b32 v93, v2 offset:3328
	ds_read_b32 v94, v2 offset:3584
	ds_read_b32 v95, v2 offset:3840
	ds_read_b32 v96, v2 offset:4096
	ds_read_b32 v97, v2 offset:4352
	ds_read_b32 v98, v2 offset:4608
	ds_read_b32 v99, v2 offset:4864
	ds_read_b32 v100, v2 offset:5120
	ds_read_b32 v101, v2 offset:5376
	ds_read_b32 v102, v2 offset:5632
	ds_read_b32 v103, v2 offset:5888
	ds_read_b32 v104, v2 offset:6144
	ds_read_b32 v105, v2 offset:6400
	ds_read_b32 v106, v2 offset:6656
	ds_read_b32 v107, v2 offset:6912
	ds_read_b32 v108, v2 offset:7168
	ds_read_b32 v109, v2 offset:7424
	ds_read_b32 v110, v2 offset:7680
	ds_read_b32 v111, v2 offset:7936
	ds_read_b32 v112, v2 offset:8192
	ds_read_b32 v113, v2 offset:8448
	ds_read_b32 v114, v2 offset:8704
	ds_read_b32 v115, v2 offset:8960
	ds_read_b32 v116, v2 offset:9216
	ds_read_b32 v117, v2 offset:9472
	ds_read_b32 v118, v2 offset:9728
	ds_read_b32 v119, v2 offset:9984
	ds_read_b32 v120, v2 offset:10240
	ds_read_b32 v121, v2 offset:10496
	ds_read_b32 v122, v2 offset:10752
	ds_read_b32 v123, v2 offset:11008
	ds_read_b32 v124, v2 offset:11264
	ds_read_b32 v125, v2 offset:11520
	ds_read_b32 v126, v2 offset:11776
	ds_read_b32 v127, v2 offset:12032
	ds_read_b32 v128, v2 offset:12288
	ds_read_b32 v129, v2 offset:12544
	ds_read_b32 v130, v2 offset:12800
	ds_read_b32 v131, v2 offset:13056
	ds_read_b32 v132, v2 offset:13312
	ds_read_b32 v133, v2 offset:13568
	ds_read_b32 v134, v2 offset:13824
	ds_read_b32 v135, v2 offset:14080
	ds_read_b32 v136, v2 offset:14336
	ds_read_b32 v137, v2 offset:14592
	ds_read_b32 v138, v2 offset:14848
	ds_read_b32 v139, v2 offset:15104
	ds_read_b32 v140, v2 offset:15360
	ds_read_b32 v141, v2 offset:15616
	ds_read_b32 v142, v2 offset:15872
	ds_read_b32 v143, v2 offset:16128
	s_add_u32 s16, s16, s18
	s_addc_u32 s17, s17, 0
	s_waitcnt lgkmcnt(0)
	v_mul_f32_e32 v6, s3, v4
	v_readlane_b32 s26, v1, 0
	v_readlane_b32 s27, v1, 1
	v_readlane_b32 s28, v1, 2
	v_readlane_b32 s29, v1, 3
	v_readlane_b32 s30, v1, 4
	v_readlane_b32 s31, v1, 5
	v_readlane_b32 s32, v1, 6
	v_readlane_b32 s33, v1, 7
	v_fmac_f32_e32 v6, s26, v80
	v_fmac_f32_e32 v6, s27, v81
	v_fmac_f32_e32 v6, s28, v82
	v_fmac_f32_e32 v6, s29, v83
	v_fmac_f32_e32 v6, s30, v84
	v_fmac_f32_e32 v6, s31, v85
	v_fmac_f32_e32 v6, s32, v86
	v_fmac_f32_e32 v6, s33, v87
	v_readlane_b32 s26, v1, 8
	v_readlane_b32 s27, v1, 9
	v_readlane_b32 s28, v1, 10
	v_readlane_b32 s29, v1, 11
	v_readlane_b32 s30, v1, 12
	v_readlane_b32 s31, v1, 13
	v_readlane_b32 s32, v1, 14
	v_readlane_b32 s33, v1, 15
	v_fmac_f32_e32 v6, s26, v88
	v_fmac_f32_e32 v6, s27, v89
	v_fmac_f32_e32 v6, s28, v90
	v_fmac_f32_e32 v6, s29, v91
	v_fmac_f32_e32 v6, s30, v92
	v_fmac_f32_e32 v6, s31, v93
	v_fmac_f32_e32 v6, s32, v94
	v_fmac_f32_e32 v6, s33, v95
	v_readlane_b32 s26, v1, 16
	v_readlane_b32 s27, v1, 17
	v_readlane_b32 s28, v1, 18
	v_readlane_b32 s29, v1, 19
	v_readlane_b32 s30, v1, 20
	v_readlane_b32 s31, v1, 21
	v_readlane_b32 s32, v1, 22
	v_readlane_b32 s33, v1, 23
	v_fmac_f32_e32 v6, s26, v96
	v_fmac_f32_e32 v6, s27, v97
	v_fmac_f32_e32 v6, s28, v98
	v_fmac_f32_e32 v6, s29, v99
	v_fmac_f32_e32 v6, s30, v100
	v_fmac_f32_e32 v6, s31, v101
	v_fmac_f32_e32 v6, s32, v102
	v_fmac_f32_e32 v6, s33, v103
	v_readlane_b32 s26, v1, 24
	v_readlane_b32 s27, v1, 25
	v_readlane_b32 s28, v1, 26
	v_readlane_b32 s29, v1, 27
	v_readlane_b32 s30, v1, 28
	v_readlane_b32 s31, v1, 29
	v_readlane_b32 s32, v1, 30
	v_readlane_b32 s33, v1, 31
	v_fmac_f32_e32 v6, s26, v104
	v_fmac_f32_e32 v6, s27, v105
	v_fmac_f32_e32 v6, s28, v106
	v_fmac_f32_e32 v6, s29, v107
	v_fmac_f32_e32 v6, s30, v108
	v_fmac_f32_e32 v6, s31, v109
	v_fmac_f32_e32 v6, s32, v110
	v_fmac_f32_e32 v6, s33, v111
	v_readlane_b32 s26, v1, 32
	v_readlane_b32 s27, v1, 33
	v_readlane_b32 s28, v1, 34
	v_readlane_b32 s29, v1, 35
	v_readlane_b32 s30, v1, 36
	v_readlane_b32 s31, v1, 37
	v_readlane_b32 s32, v1, 38
	v_readlane_b32 s33, v1, 39
	v_fmac_f32_e32 v6, s26, v112
	v_fmac_f32_e32 v6, s27, v113
	v_fmac_f32_e32 v6, s28, v114
	v_fmac_f32_e32 v6, s29, v115
	v_fmac_f32_e32 v6, s30, v116
	v_fmac_f32_e32 v6, s31, v117
	v_fmac_f32_e32 v6, s32, v118
	v_fmac_f32_e32 v6, s33, v119
	v_readlane_b32 s26, v1, 40
	v_readlane_b32 s27, v1, 41
	v_readlane_b32 s28, v1, 42
	v_readlane_b32 s29, v1, 43
	v_readlane_b32 s30, v1, 44
	v_readlane_b32 s31, v1, 45
	v_readlane_b32 s32, v1, 46
	v_readlane_b32 s33, v1, 47
	v_fmac_f32_e32 v6, s26, v120
	v_fmac_f32_e32 v6, s27, v121
	v_fmac_f32_e32 v6, s28, v122
	v_fmac_f32_e32 v6, s29, v123
	v_fmac_f32_e32 v6, s30, v124
	v_fmac_f32_e32 v6, s31, v125
	v_fmac_f32_e32 v6, s32, v126
	v_fmac_f32_e32 v6, s33, v127
	v_readlane_b32 s26, v1, 48
	v_readlane_b32 s27, v1, 49
	v_readlane_b32 s28, v1, 50
	v_readlane_b32 s29, v1, 51
	v_readlane_b32 s30, v1, 52
	v_readlane_b32 s31, v1, 53
	v_readlane_b32 s32, v1, 54
	v_readlane_b32 s33, v1, 55
	v_fmac_f32_e32 v6, s26, v128
	v_fmac_f32_e32 v6, s27, v129
	v_fmac_f32_e32 v6, s28, v130
	v_fmac_f32_e32 v6, s29, v131
	v_fmac_f32_e32 v6, s30, v132
	v_fmac_f32_e32 v6, s31, v133
	v_fmac_f32_e32 v6, s32, v134
	v_fmac_f32_e32 v6, s33, v135
	v_readlane_b32 s26, v1, 56
	v_readlane_b32 s27, v1, 57
	v_readlane_b32 s28, v1, 58
	v_readlane_b32 s29, v1, 59
	v_readlane_b32 s30, v1, 60
	v_readlane_b32 s31, v1, 61
	v_readlane_b32 s32, v1, 62
	v_readlane_b32 s33, v1, 63
	v_fmac_f32_e32 v6, s26, v136
	v_fmac_f32_e32 v6, s27, v137
	v_fmac_f32_e32 v6, s28, v138
	v_fmac_f32_e32 v6, s29, v139
	v_fmac_f32_e32 v6, s30, v140
	v_fmac_f32_e32 v6, s31, v141
	v_fmac_f32_e32 v6, s32, v142
	v_fmac_f32_e32 v6, s33, v143
	v_max_f32_e64 v7, s3, s3
	v_max_f32_e32 v7, 1.0, v7
	ds_read_b32 v80, v2 offset:16384
	ds_read_b32 v81, v2 offset:16424
	ds_read_b32 v82, v2 offset:16464
	ds_read_b32 v83, v2 offset:16504
	ds_read_b32 v84, v2 offset:16544
	ds_read_b32 v85, v2 offset:16584
	ds_read_b32 v86, v2 offset:16624
	ds_read_b32 v87, v2 offset:16664
	ds_read_b32 v88, v2 offset:16704
	ds_read_b32 v89, v2 offset:16744
	ds_read_b32 v90, v2 offset:16784
	ds_read_b32 v91, v2 offset:16824
	ds_read_b32 v92, v2 offset:16864
	ds_read_b32 v93, v2 offset:16904
	ds_read_b32 v94, v2 offset:16944
	ds_read_b32 v95, v2 offset:16984
	ds_read_b32 v96, v2 offset:17024
	ds_read_b32 v97, v2 offset:17064
	ds_read_b32 v98, v2 offset:17104
	ds_read_b32 v99, v2 offset:17144
	ds_read_b32 v100, v2 offset:17184
	ds_read_b32 v101, v2 offset:17224
	ds_read_b32 v102, v2 offset:17264
	ds_read_b32 v103, v2 offset:17304
	ds_read_b32 v104, v2 offset:17344
	ds_read_b32 v105, v2 offset:17384
	ds_read_b32 v106, v2 offset:17424
	ds_read_b32 v107, v2 offset:17464
	ds_read_b32 v108, v2 offset:17504
	ds_read_b32 v109, v2 offset:17544
	ds_read_b32 v110, v2 offset:17584
	ds_read_b32 v111, v2 offset:17624
	ds_read_b32 v112, v2 offset:17664
	ds_read_b32 v113, v2 offset:17704
	ds_read_b32 v114, v2 offset:17744
	ds_read_b32 v115, v2 offset:17784
	ds_read_b32 v116, v2 offset:17824
	ds_read_b32 v117, v2 offset:17864
	ds_read_b32 v118, v2 offset:17904
	ds_read_b32 v119, v2 offset:17944
	ds_read_b32 v120, v2 offset:17984
	ds_read_b32 v121, v2 offset:18024
	ds_read_b32 v122, v2 offset:18064
	ds_read_b32 v123, v2 offset:18104
	ds_read_b32 v124, v2 offset:18144
	ds_read_b32 v125, v2 offset:18184
	ds_read_b32 v126, v2 offset:18224
	ds_read_b32 v127, v2 offset:18264
	ds_read_b32 v128, v2 offset:18304
	ds_read_b32 v129, v2 offset:18344
	ds_read_b32 v130, v2 offset:18384
	ds_read_b32 v131, v2 offset:18424
	ds_read_b32 v132, v2 offset:18464
	ds_read_b32 v133, v2 offset:18504
	ds_read_b32 v134, v2 offset:18544
	ds_read_b32 v135, v2 offset:18584
	ds_read_b32 v136, v2 offset:18624
	ds_read_b32 v137, v2 offset:18664
	ds_read_b32 v138, v2 offset:18704
	ds_read_b32 v139, v2 offset:18744
	ds_read_b32 v140, v2 offset:18784
	ds_read_b32 v141, v2 offset:18824
	ds_read_b32 v142, v2 offset:18864
	ds_read_b32 v143, v2 offset:18904
	v_div_scale_f32 v10, s[34:35], v7, v7, v6
	v_rcp_f32_e32 v11, v10
	v_div_scale_f32 v12, vcc, v6, v7, v6
	v_fma_f32 v13, -v10, v11, 1.0
	v_fmac_f32_e32 v11, v13, v11
	v_mul_f32_e32 v13, v12, v11
	v_fma_f32 v14, -v10, v13, v12
	v_fmac_f32_e32 v13, v14, v11
	v_fma_f32 v10, -v10, v13, v12
	v_div_fmas_f32 v10, v10, v11, v13
	v_div_fixup_f32 v6, v10, v7, v6
	s_waitcnt vmcnt(0) lgkmcnt(0)
	v_readlane_b32 s26, v6, 0
	v_readlane_b32 s27, v6, 1
	v_readlane_b32 s28, v6, 2
	v_readlane_b32 s29, v6, 3
	v_readlane_b32 s30, v6, 4
	v_readlane_b32 s31, v6, 5
	v_readlane_b32 s32, v6, 6
	v_readlane_b32 s33, v6, 7
	v_fmac_f32_e32 v5, s26, v80
	v_fmac_f32_e32 v5, s27, v81
	v_fmac_f32_e32 v5, s28, v82
	v_fmac_f32_e32 v5, s29, v83
	v_fmac_f32_e32 v5, s30, v84
	v_fmac_f32_e32 v5, s31, v85
	v_fmac_f32_e32 v5, s32, v86
	v_fmac_f32_e32 v5, s33, v87
	v_readlane_b32 s26, v6, 8
	v_readlane_b32 s27, v6, 9
	v_readlane_b32 s28, v6, 10
	v_readlane_b32 s29, v6, 11
	v_readlane_b32 s30, v6, 12
	v_readlane_b32 s31, v6, 13
	v_readlane_b32 s32, v6, 14
	v_readlane_b32 s33, v6, 15
	v_fmac_f32_e32 v5, s26, v88
	v_fmac_f32_e32 v5, s27, v89
	v_fmac_f32_e32 v5, s28, v90
	v_fmac_f32_e32 v5, s29, v91
	v_fmac_f32_e32 v5, s30, v92
	v_fmac_f32_e32 v5, s31, v93
	v_fmac_f32_e32 v5, s32, v94
	v_fmac_f32_e32 v5, s33, v95
	v_readlane_b32 s26, v6, 16
	v_readlane_b32 s27, v6, 17
	v_readlane_b32 s28, v6, 18
	v_readlane_b32 s29, v6, 19
	v_readlane_b32 s30, v6, 20
	v_readlane_b32 s31, v6, 21
	v_readlane_b32 s32, v6, 22
	v_readlane_b32 s33, v6, 23
	v_fmac_f32_e32 v5, s26, v96
	v_fmac_f32_e32 v5, s27, v97
	v_fmac_f32_e32 v5, s28, v98
	v_fmac_f32_e32 v5, s29, v99
	v_fmac_f32_e32 v5, s30, v100
	v_fmac_f32_e32 v5, s31, v101
	v_fmac_f32_e32 v5, s32, v102
	v_fmac_f32_e32 v5, s33, v103
	v_readlane_b32 s26, v6, 24
	v_readlane_b32 s27, v6, 25
	v_readlane_b32 s28, v6, 26
	v_readlane_b32 s29, v6, 27
	v_readlane_b32 s30, v6, 28
	v_readlane_b32 s31, v6, 29
	v_readlane_b32 s32, v6, 30
	v_readlane_b32 s33, v6, 31
	v_fmac_f32_e32 v5, s26, v104
	v_fmac_f32_e32 v5, s27, v105
	v_fmac_f32_e32 v5, s28, v106
	v_fmac_f32_e32 v5, s29, v107
	v_fmac_f32_e32 v5, s30, v108
	v_fmac_f32_e32 v5, s31, v109
	v_fmac_f32_e32 v5, s32, v110
	v_fmac_f32_e32 v5, s33, v111
	v_readlane_b32 s26, v6, 32
	v_readlane_b32 s27, v6, 33
	v_readlane_b32 s28, v6, 34
	v_readlane_b32 s29, v6, 35
	v_readlane_b32 s30, v6, 36
	v_readlane_b32 s31, v6, 37
	v_readlane_b32 s32, v6, 38
	v_readlane_b32 s33, v6, 39
	v_fmac_f32_e32 v5, s26, v112
	v_fmac_f32_e32 v5, s27, v113
	v_fmac_f32_e32 v5, s28, v114
	v_fmac_f32_e32 v5, s29, v115
	v_fmac_f32_e32 v5, s30, v116
	v_fmac_f32_e32 v5, s31, v117
	v_fmac_f32_e32 v5, s32, v118
	v_fmac_f32_e32 v5, s33, v119
	v_readlane_b32 s26, v6, 40
	v_readlane_b32 s27, v6, 41
	v_readlane_b32 s28, v6, 42
	v_readlane_b32 s29, v6, 43
	v_readlane_b32 s30, v6, 44
	v_readlane_b32 s31, v6, 45
	v_readlane_b32 s32, v6, 46
	v_readlane_b32 s33, v6, 47
	v_fmac_f32_e32 v5, s26, v120
	v_fmac_f32_e32 v5, s27, v121
	v_fmac_f32_e32 v5, s28, v122
	v_fmac_f32_e32 v5, s29, v123
	v_fmac_f32_e32 v5, s30, v124
	v_fmac_f32_e32 v5, s31, v125
	v_fmac_f32_e32 v5, s32, v126
	v_fmac_f32_e32 v5, s33, v127
	v_readlane_b32 s26, v6, 48
	v_readlane_b32 s27, v6, 49
	v_readlane_b32 s28, v6, 50
	v_readlane_b32 s29, v6, 51
	v_readlane_b32 s30, v6, 52
	v_readlane_b32 s31, v6, 53
	v_readlane_b32 s32, v6, 54
	v_readlane_b32 s33, v6, 55
	v_fmac_f32_e32 v5, s26, v128
	v_fmac_f32_e32 v5, s27, v129
	v_fmac_f32_e32 v5, s28, v130
	v_fmac_f32_e32 v5, s29, v131
	v_fmac_f32_e32 v5, s30, v132
	v_fmac_f32_e32 v5, s31, v133
	v_fmac_f32_e32 v5, s32, v134
	v_fmac_f32_e32 v5, s33, v135
	v_readlane_b32 s26, v6, 56
	v_readlane_b32 s27, v6, 57
	v_readlane_b32 s28, v6, 58
	v_readlane_b32 s29, v6, 59
	v_readlane_b32 s30, v6, 60
	v_readlane_b32 s31, v6, 61
	v_readlane_b32 s32, v6, 62
	v_readlane_b32 s33, v6, 63
	v_fmac_f32_e32 v5, s26, v136
	v_fmac_f32_e32 v5, s27, v137
	v_fmac_f32_e32 v5, s28, v138
	v_fmac_f32_e32 v5, s29, v139
	v_fmac_f32_e32 v5, s30, v140
	v_fmac_f32_e32 v5, s31, v141
	v_fmac_f32_e32 v5, s32, v142
	v_fmac_f32_e32 v5, s33, v143
	v_cmp_gt_u32_e32 vcc, 10, v0
	s_and_saveexec_b64 s[20:21], vcc
	s_cbranch_execz .Lfinal_done
	global_store_dword v2, v5, s[16:17]

	.amdhsa_kernel _Z7k_finalPKfS0_S0_S0_S0_S0_Pf
		.amdhsa_group_segment_fixed_size 20480
		.amdhsa_private_segment_fixed_size 0
		.amdhsa_kernarg_size 56
		.amdhsa_user_sgpr_count 2
		.amdhsa_user_sgpr_dispatch_ptr 0
		.amdhsa_user_sgpr_queue_ptr 0
		.amdhsa_user_sgpr_kernarg_segment_ptr 1
		.amdhsa_user_sgpr_dispatch_id 0
		.amdhsa_user_sgpr_kernarg_preload_length 0
		.amdhsa_user_sgpr_kernarg_preload_offset 0
		.amdhsa_user_sgpr_private_segment_size 0
		.amdhsa_uses_dynamic_stack 0
		.amdhsa_enable_private_segment 0
		.amdhsa_system_sgpr_workgroup_id_x 1
		.amdhsa_system_sgpr_workgroup_id_y 0
		.amdhsa_system_sgpr_workgroup_id_z 0
		.amdhsa_system_sgpr_workgroup_info 0
		.amdhsa_system_vgpr_workitem_id 0
		.amdhsa_next_free_vgpr 144
		.amdhsa_next_free_sgpr 36
		.amdhsa_accum_offset 144
		.amdhsa_reserve_vcc 1
		.amdhsa_float_round_mode_32 0
		.amdhsa_float_round_mode_16_64 0
		.amdhsa_float_denorm_mode_32 3
		.amdhsa_float_denorm_mode_16_64 3
		.amdhsa_dx10_clamp 1
		.amdhsa_ieee_mode 1
		.amdhsa_fp16_overflow 0
		.amdhsa_tg_split 0
		.amdhsa_exception_fp_ieee_invalid_op 0
		.amdhsa_exception_fp_denorm_src 0
		.amdhsa_exception_fp_ieee_div_zero 0
		.amdhsa_exception_fp_ieee_overflow 0
		.amdhsa_exception_fp_ieee_underflow 0
		.amdhsa_exception_fp_ieee_inexact 0
		.amdhsa_exception_int_div_zero 0
	.end_amdhsa_kernel

	.text
	.protected	_Z6k_nodeILi0ELi0EEvPfS0_PDv2_DF16_PKiPKfS4_S0_S0_S4_S6_PKDv8_DF16_S6_S9_S6_S9_
	.globl	_Z6k_nodeILi0ELi0EEvPfS0_PDv2_DF16_PKiPKfS4_S0_S0_S4_S6_PKDv8_DF16_S6_S9_S6_S9_
	.p2align	8
	.type	_Z6k_nodeILi0ELi0EEvPfS0_PDv2_DF16_PKiPKfS4_S0_S0_S4_S6_PKDv8_DF16_S6_S9_S6_S9_,@function
_Z6k_nodeILi0ELi0EEvPfS0_PDv2_DF16_PKiPKfS4_S0_S0_S4_S6_PKDv8_DF16_S6_S9_S6_S9_:
	s_load_dwordx8 s[4:11], s[0:1], 0x40
	s_load_dwordx4 s[24:27], s[0:1], 0x18
	v_mov_b32_e32 v111, 0
	v_lshlrev_b32_e32 v112, 4, v0
	v_mov_b32_e32 v113, v111
	s_waitcnt lgkmcnt(0)
	v_lshl_add_u64 v[2:3], s[8:9], 0, v[112:113]
	v_add_co_u32_e32 v2, vcc, 0x1000, v2
	s_nop 1
	v_addc_co_u32_e32 v3, vcc, 0, v3, vcc
	global_load_dwordx4 v[54:57], v112, s[8:9]
	global_load_dwordx4 v[50:53], v[2:3], off
	s_load_dwordx2 s[14:15], s[0:1], 0x70
	s_load_dwordx2 s[12:13], s[0:1], 0x0
	s_waitcnt lgkmcnt(0)
	s_cmp_lg_u64 s[14:15], 0
	s_cselect_b64 s[8:9], -1, 0
	s_cmp_eq_u64 s[14:15], 0
	s_cbranch_scc1 .LBB7_2
	v_mov_b32_e32 v1, 0x1000
	v_lshl_or_b32 v1, v0, 4, v1
	global_load_dwordx4 v[102:105], v112, s[14:15]
	global_load_dwordx4 v[98:101], v1, s[14:15]
	s_branch .LBB7_3

.LBB7_3:
	v_lshrrev_b32_e32 v1, 6, v0
	v_lshl_or_b32 v106, s2, 2, v1
	v_and_b32_e32 v107, 31, v0
	v_lshlrev_b32_e32 v114, 5, v106
	v_or_b32_e32 v2, v114, v107
	v_min_i32_e32 v58, 0xc34f, v2
	v_ashrrev_i32_e32 v59, 31, v58
	v_lshl_add_u64 v[2:3], v[58:59], 2, s[4:5]
	global_load_dwordx2 v[108:109], v[2:3], off
	v_lshl_add_u64 v[154:155], v[58:59], 2, s[24:25]
	global_load_dword v154, v[154:155], off
	v_min_i32_e32 v2, 0x61a, v106
	v_lshlrev_b32_e32 v3, 5, v2
	v_sub_u32_e32 v3, 0xc350, v3
	v_min_u32_e32 v3, 32, v3
	v_add_u32_e32 v8, -1, v3
	v_ashrrev_i32_e32 v3, 31, v2
	v_lshlrev_b32_e32 v4, 2, v0
	v_and_b32_e32 v143, 60, v4
	v_bfe_u32 v142, v0, 4, 2
	v_lshlrev_b64 v[2:3], 13, v[2:3]
	v_lshl_add_u64 v[2:3], s[12:13], 0, v[2:3]
	v_lshlrev_b32_e32 v110, 2, v143
	v_or_b32_e32 v140, 4, v142
	v_lshl_add_u64 v[2:3], v[2:3], 0, v[110:111]
	v_lshlrev_b32_e32 v4, 8, v142
	v_mov_b32_e32 v5, v111
	v_lshlrev_b32_e32 v6, 8, v140
	v_mov_b32_e32 v7, v111
	v_lshl_add_u64 v[4:5], v[2:3], 0, v[4:5]
	v_lshl_add_u64 v[6:7], v[2:3], 0, v[6:7]
	v_or_b32_e32 v139, 8, v142
	v_or_b32_e32 v138, 12, v142
	global_load_dwordx4 v[34:37], v[4:5], off
	global_load_dwordx4 v[38:41], v[6:7], off
	v_lshlrev_b32_e32 v4, 8, v139
	v_mov_b32_e32 v5, v111
	v_lshlrev_b32_e32 v6, 8, v138
	v_mov_b32_e32 v7, v111
	v_lshl_add_u64 v[4:5], v[2:3], 0, v[4:5]
	v_lshl_add_u64 v[6:7], v[2:3], 0, v[6:7]
	v_or_b32_e32 v137, 16, v142
	v_or_b32_e32 v136, 20, v142
	global_load_dwordx4 v[42:45], v[4:5], off
	global_load_dwordx4 v[46:49], v[6:7], off
	v_min_u32_e32 v4, v137, v8
	v_min_u32_e32 v6, v136, v8
	v_lshlrev_b32_e32 v4, 8, v4
	v_mov_b32_e32 v5, v111
	v_lshlrev_b32_e32 v6, 8, v6
	v_mov_b32_e32 v7, v111
	v_lshl_add_u64 v[4:5], v[2:3], 0, v[4:5]
	v_lshl_add_u64 v[6:7], v[2:3], 0, v[6:7]
	v_or_b32_e32 v135, 24, v142
	v_or_b32_e32 v134, 28, v142
	global_load_dwordx4 v[82:85], v[4:5], off
	global_load_dwordx4 v[86:89], v[6:7], off
	v_min_u32_e32 v4, v135, v8
	v_min_u32_e32 v6, v134, v8
	v_bfe_u32 v113, v0, 5, 1
	v_lshlrev_b32_e32 v4, 8, v4
	v_mov_b32_e32 v5, v111
	v_lshlrev_b32_e32 v6, 8, v6
	v_mov_b32_e32 v7, v111
	v_lshl_add_u64 v[4:5], v[2:3], 0, v[4:5]
	v_lshl_add_u64 v[2:3], v[2:3], 0, v[6:7]
	v_lshlrev_b32_e32 v144, 4, v113
	global_load_dwordx4 v[90:93], v[4:5], off
	global_load_dwordx4 v[94:97], v[2:3], off
	global_load_dwordx4 v[18:21], v144, s[10:11]
	global_load_dwordx4 v[22:25], v144, s[10:11] offset:32
	global_load_dwordx4 v[26:29], v144, s[10:11] offset:64
	global_load_dwordx4 v[30:33], v144, s[10:11] offset:96
	s_nop 0
	global_load_dwordx4 v[2:5], v144, s[10:11] offset:128
	global_load_dwordx4 v[6:9], v144, s[10:11] offset:160
	global_load_dwordx4 v[10:13], v144, s[10:11] offset:192
	global_load_dwordx4 v[14:17], v144, s[10:11] offset:224
	s_load_dwordx2 s[20:21], s[0:1], 0x10
	s_waitcnt vmcnt(18)
	ds_write_b128 v112, v[54:57] offset:34816
	v_cndmask_b32_e64 v54, 0, 1, s[8:9]
	v_cmp_ne_u32_e64 s[18:19], 1, v54
	s_andn2_b64 vcc, exec, s[8:9]
	s_waitcnt vmcnt(17)
	ds_write_b128 v112, v[50:53] offset:38912
	s_cbranch_vccnz .LBB7_5
	s_load_dwordx4 s[8:11], s[0:1], 0x18
	v_add_u32_e32 v111, 0x8800, v112
	s_waitcnt lgkmcnt(0)
	s_nop 0
	s_nop 0
	v_lshlrev_b32_e32 v50, 2, v113
	v_mov_b32_e32 v51, 0
	v_lshlrev_b32_e32 v50, 2, v50
	s_waitcnt vmcnt(16)
	v_lshlrev_b32_e32 v52, 6, v154
	v_ashrrev_i32_e32 v53, 31, v52
	v_lshl_add_u64 v[52:53], v[52:53], 2, s[10:11]
	v_lshl_add_u64 v[116:117], v[52:53], 0, v[50:51]
	global_load_dwordx4 v[74:77], v[116:117], off
	global_load_dwordx4 v[78:81], v[116:117], off offset:32
	global_load_dwordx4 v[70:73], v[116:117], off offset:64
	global_load_dwordx4 v[66:69], v[116:117], off offset:96
	global_load_dwordx4 v[62:65], v[116:117], off offset:128
	global_load_dwordx4 v[58:61], v[116:117], off offset:160
	global_load_dwordx4 v[54:57], v[116:117], off offset:192
	global_load_dwordx4 v[50:53], v[116:117], off offset:224
	ds_write_b128 v111, v[102:105] offset:16384
	ds_write_b128 v111, v[98:101] offset:20480
	s_branch .LBB7_6
.LBB7_5:
	s_waitcnt vmcnt(17)
.LBB7_6:
	s_nop 0
	v_ashrrev_i32_e32 v150, 5, v108
	v_add_u32_e32 v98, 1, v150
	v_sub_u32_e32 v146, 0xc350, v114
	v_lshlrev_b32_e32 v99, 5, v98
	v_cmp_gt_i32_e32 vcc, v146, v107
	v_cmp_lt_i32_e64 s[2:3], v99, v109
	v_ashrrev_i32_e32 v99, 31, v98
	v_lshlrev_b64 v[98:99], 6, v[98:99]
	s_and_b64 vcc, vcc, s[2:3]
	v_cndmask_b32_e32 v99, 0, v99, vcc
	v_cndmask_b32_e32 v98, 0, v98, vcc
	v_lshl_add_u64 v[98:99], v[98:99], 2, s[6:7]
	v_lshlrev_b32_e32 v128, 5, v113
	v_mov_b32_e32 v129, 0
	v_lshl_add_u64 v[130:131], v[98:99], 0, v[128:129]
	global_load_dwordx4 v[98:101], v[130:131], off
	global_load_dwordx4 v[102:105], v[130:131], off offset:16
	global_load_dwordx4 v[112:115], v[130:131], off offset:64
	global_load_dwordx4 v[116:119], v[130:131], off offset:80
	global_load_dwordx4 v[120:123], v[130:131], off offset:128
	global_load_dwordx4 v[124:127], v[130:131], off offset:144
	v_mul_u32_u24_e32 v145, 0x2200, v1
	v_mul_u32_u24_e32 v141, 0x110, v142
	v_add3_u32 v110, v145, v141, v110
	s_waitcnt vmcnt(21)
	ds_write_b128 v110, v[34:37]
	s_waitcnt vmcnt(20)
	ds_write_b128 v110, v[38:41] offset:1088
	s_waitcnt vmcnt(19)
	ds_write_b128 v110, v[42:45] offset:2176
	s_waitcnt vmcnt(18)
	ds_write_b128 v110, v[46:49] offset:3264
	s_waitcnt vmcnt(17)
	ds_write_b128 v110, v[82:85] offset:4352
	s_waitcnt vmcnt(16)
	ds_write_b128 v110, v[86:89] offset:5440
	s_waitcnt vmcnt(15)
	ds_write_b128 v110, v[90:93] offset:6528
	s_waitcnt vmcnt(14)
	ds_write_b128 v110, v[94:97] offset:7616
	global_load_dwordx4 v[34:37], v[130:131], off offset:208
	global_load_dwordx4 v[38:41], v[130:131], off offset:192
	s_load_dwordx2 s[2:3], s[0:1], 0x8
	s_movk_i32 s0, 0x2200
	v_mul_u32_u24_e32 v107, 0x110, v107
	v_mad_u32_u24 v148, v1, s0, v107
	v_add_u32_e32 v1, v148, v128
	s_waitcnt lgkmcnt(0)
	s_barrier
	ds_read_b128 v[42:45], v1
	ds_read_b128 v[46:49], v1 offset:16
	ds_read_b128 v[82:85], v1 offset:64
	ds_read_b128 v[86:89], v1 offset:80
	v_cmp_eq_u32_e64 s[0:1], v108, v109
	v_ashrrev_i32_e32 v151, 31, v150
	v_and_b32_e32 v147, 63, v0
	s_mov_b64 s[4:5], 0x200
	s_waitcnt vmcnt(7) lgkmcnt(3)
	v_add_f32_e32 v90, v42, v98
	v_add_f32_e32 v91, v43, v99
	v_add_f32_e32 v92, v44, v100
	v_add_f32_e32 v93, v45, v101
	s_waitcnt vmcnt(6) lgkmcnt(2)
	v_add_f32_e32 v96, v48, v104
	s_waitcnt vmcnt(4) lgkmcnt(0)
	v_add_f32_e32 v107, v88, v118
	v_cndmask_b32_e32 v42, v42, v90, vcc
	v_add_f32_e32 v97, v49, v105
	v_add_f32_e32 v98, v82, v112
	v_add_f32_e32 v99, v83, v113
	v_cndmask_b32_e32 v43, v43, v91, vcc
	v_cndmask_b32_e32 v44, v44, v92, vcc
	v_cndmask_b32_e32 v45, v45, v93, vcc
	v_cndmask_b32_e32 v48, v48, v96, vcc
	v_cndmask_b32_e64 v96, v42, 0, s[0:1]
	v_cndmask_b32_e32 v42, v88, v107, vcc
	v_add_f32_e32 v94, v46, v102
	v_add_f32_e32 v102, v86, v116
	v_cndmask_b32_e32 v49, v49, v97, vcc
	v_cndmask_b32_e32 v82, v82, v98, vcc
	v_cndmask_b32_e32 v83, v83, v99, vcc
	v_cndmask_b32_e64 v97, v43, 0, s[0:1]
	v_cndmask_b32_e64 v98, v44, 0, s[0:1]
	v_cndmask_b32_e64 v99, v45, 0, s[0:1]
	v_cndmask_b32_e64 v116, v42, 0, s[0:1]
	ds_read_b128 v[42:45], v1 offset:128
	v_add_f32_e32 v100, v84, v114
	v_cndmask_b32_e32 v46, v46, v94, vcc
	v_add_f32_e32 v95, v47, v103
	v_cndmask_b32_e32 v84, v84, v100, vcc
	v_cndmask_b32_e64 v100, v46, 0, s[0:1]
	v_add_f32_e32 v46, v89, v119
	v_add_f32_e32 v101, v85, v115
	v_add_f32_e32 v103, v87, v117
	v_cndmask_b32_e32 v47, v47, v95, vcc
	v_cndmask_b32_e32 v46, v89, v46, vcc
	v_cndmask_b32_e32 v85, v85, v101, vcc
	v_cndmask_b32_e32 v86, v86, v102, vcc
	v_cndmask_b32_e32 v87, v87, v103, vcc
	v_cndmask_b32_e64 v101, v47, 0, s[0:1]
	v_cndmask_b32_e64 v102, v48, 0, s[0:1]
	v_cndmask_b32_e64 v103, v49, 0, s[0:1]
	v_cndmask_b32_e64 v104, v82, 0, s[0:1]
	v_cndmask_b32_e64 v117, v46, 0, s[0:1]
	ds_read_b128 v[46:49], v1 offset:144
	s_waitcnt vmcnt(3) lgkmcnt(1)
	v_add_f32_e32 v82, v42, v120
	v_cndmask_b32_e32 v42, v42, v82, vcc
	v_cndmask_b32_e64 v118, v42, 0, s[0:1]
	v_add_f32_e32 v42, v43, v121
	v_cndmask_b32_e32 v42, v43, v42, vcc
	v_cndmask_b32_e64 v119, v42, 0, s[0:1]
	v_add_f32_e32 v42, v44, v122
	v_cndmask_b32_e32 v42, v44, v42, vcc
	v_cndmask_b32_e64 v120, v42, 0, s[0:1]
	v_add_f32_e32 v42, v45, v123
	v_cndmask_b32_e32 v42, v45, v42, vcc
	v_cndmask_b32_e64 v121, v42, 0, s[0:1]
	s_waitcnt vmcnt(2) lgkmcnt(0)
	v_add_f32_e32 v42, v46, v124
	v_cndmask_b32_e32 v42, v46, v42, vcc
	v_cndmask_b32_e64 v122, v42, 0, s[0:1]
	v_add_f32_e32 v42, v47, v125
	v_cndmask_b32_e32 v42, v47, v42, vcc
	v_cndmask_b32_e64 v123, v42, 0, s[0:1]
	v_add_f32_e32 v42, v48, v126
	v_cndmask_b32_e32 v42, v48, v42, vcc
	v_cndmask_b32_e64 v124, v42, 0, s[0:1]
	ds_read_b128 v[42:45], v1 offset:192
	v_add_f32_e32 v46, v49, v127
	v_cndmask_b32_e32 v46, v49, v46, vcc
	v_cndmask_b32_e64 v125, v46, 0, s[0:1]
	ds_read_b128 v[46:49], v1 offset:208
	s_waitcnt vmcnt(0) lgkmcnt(1)
	v_add_f32_e32 v1, v42, v38
	v_cndmask_b32_e32 v1, v42, v1, vcc
	v_cndmask_b32_e64 v126, v1, 0, s[0:1]
	v_add_f32_e32 v1, v43, v39
	v_cndmask_b32_e32 v1, v43, v1, vcc
	v_cndmask_b32_e64 v127, v1, 0, s[0:1]
	v_add_f32_e32 v1, v44, v40
	v_cndmask_b32_e32 v1, v44, v1, vcc
	v_cndmask_b32_e64 v128, v1, 0, s[0:1]
	v_add_f32_e32 v1, v45, v41
	v_cndmask_b32_e32 v1, v45, v1, vcc
	v_cndmask_b32_e64 v129, v1, 0, s[0:1]
	s_waitcnt lgkmcnt(0)
	v_add_f32_e32 v1, v46, v34
	v_cndmask_b32_e32 v1, v46, v1, vcc
	v_cndmask_b32_e64 v130, v1, 0, s[0:1]
	v_add_f32_e32 v1, v47, v35
	v_cndmask_b32_e32 v1, v47, v1, vcc
	v_cndmask_b32_e64 v131, v1, 0, s[0:1]
	v_add_f32_e32 v1, v48, v36
	v_cndmask_b32_e32 v1, v48, v1, vcc
	v_cndmask_b32_e64 v132, v1, 0, s[0:1]
	v_add_f32_e32 v1, v49, v37
	v_cndmask_b32_e32 v1, v49, v1, vcc
	v_cndmask_b32_e64 v133, v1, 0, s[0:1]
	v_and_b32_e32 v1, 0xffffffe0, v108
	v_add_u32_e32 v34, 64, v1
	v_cndmask_b32_e64 v105, v83, 0, s[0:1]
	v_cndmask_b32_e64 v112, v84, 0, s[0:1]
	v_cndmask_b32_e64 v113, v85, 0, s[0:1]
	v_cndmask_b32_e64 v114, v86, 0, s[0:1]
	v_cndmask_b32_e64 v115, v87, 0, s[0:1]
	v_cmp_lt_i32_e64 s[0:1], v34, v109
	v_lshlrev_b64 v[34:35], 8, v[150:151]
	v_and_or_b32 v34, v0, 32, v34
	v_add_u32_e32 v107, 0x60, v1
	v_lshl_add_u64 v[0:1], s[6:7], 0, v[34:35]
	s_and_b64 s[0:1], vcc, s[0:1]
	v_lshl_add_u64 v[110:111], v[0:1], 0, s[4:5]
	s_mov_b64 s[4:5], 0x100
	s_branch .LBB7_9

	.amdhsa_kernel _Z6k_nodeILi0ELi0EEvPfS0_PDv2_DF16_PKiPKfS4_S0_S0_S4_S6_PKDv8_DF16_S6_S9_S6_S9_
		.amdhsa_group_segment_fixed_size 59392
		.amdhsa_private_segment_fixed_size 0
		.amdhsa_kernarg_size 120
		.amdhsa_user_sgpr_count 2
		.amdhsa_user_sgpr_dispatch_ptr 0
		.amdhsa_user_sgpr_queue_ptr 0
		.amdhsa_user_sgpr_kernarg_segment_ptr 1
		.amdhsa_user_sgpr_dispatch_id 0
		.amdhsa_user_sgpr_kernarg_preload_length 0
		.amdhsa_user_sgpr_kernarg_preload_offset 0
		.amdhsa_user_sgpr_private_segment_size 0
		.amdhsa_uses_dynamic_stack 0
		.amdhsa_enable_private_segment 0
		.amdhsa_system_sgpr_workgroup_id_x 1
		.amdhsa_system_sgpr_workgroup_id_y 0
		.amdhsa_system_sgpr_workgroup_id_z 0
		.amdhsa_system_sgpr_workgroup_info 0
		.amdhsa_system_vgpr_workitem_id 0
		.amdhsa_next_free_vgpr 169
		.amdhsa_next_free_sgpr 96
		.amdhsa_accum_offset 156
		.amdhsa_reserve_vcc 1
		.amdhsa_float_round_mode_32 0
		.amdhsa_float_round_mode_16_64 0
		.amdhsa_float_denorm_mode_32 3
		.amdhsa_float_denorm_mode_16_64 3
		.amdhsa_dx10_clamp 1
		.amdhsa_ieee_mode 1
		.amdhsa_fp16_overflow 0
		.amdhsa_tg_split 0
		.amdhsa_exception_fp_ieee_invalid_op 0
		.amdhsa_exception_fp_denorm_src 0
		.amdhsa_exception_fp_ieee_div_zero 0
		.amdhsa_exception_fp_ieee_overflow 0
		.amdhsa_exception_fp_ieee_underflow 0
		.amdhsa_exception_fp_ieee_inexact 0
		.amdhsa_exception_int_div_zero 0
	.end_amdhsa_kernel
	.text
.Lfunc_end7:
	.size	_Z6k_nodeILi0ELi0EEvPfS0_PDv2_DF16_PKiPKfS4_S0_S0_S4_S6_PKDv8_DF16_S6_S9_S6_S9_, .Lfunc_end7-_Z6k_nodeILi0ELi0EEvPfS0_PDv2_DF16_PKiPKfS4_S0_S0_S4_S6_PKDv8_DF16_S6_S9_S6_S9_
	.set _Z6k_nodeILi0ELi0EEvPfS0_PDv2_DF16_PKiPKfS4_S0_S0_S4_S6_PKDv8_DF16_S6_S9_S6_S9_.num_vgpr, 154
	.set _Z6k_nodeILi0ELi0EEvPfS0_PDv2_DF16_PKiPKfS4_S0_S0_S4_S6_PKDv8_DF16_S6_S9_S6_S9_.num_agpr, 0
	.set _Z6k_nodeILi0ELi0EEvPfS0_PDv2_DF16_PKiPKfS4_S0_S0_S4_S6_PKDv8_DF16_S6_S9_S6_S9_.numbered_sgpr, 24
	.set _Z6k_nodeILi0ELi0EEvPfS0_PDv2_DF16_PKiPKfS4_S0_S0_S4_S6_PKDv8_DF16_S6_S9_S6_S9_.num_named_barrier, 0
	.set _Z6k_nodeILi0ELi0EEvPfS0_PDv2_DF16_PKiPKfS4_S0_S0_S4_S6_PKDv8_DF16_S6_S9_S6_S9_.private_seg_size, 0
	.set _Z6k_nodeILi0ELi0EEvPfS0_PDv2_DF16_PKiPKfS4_S0_S0_S4_S6_PKDv8_DF16_S6_S9_S6_S9_.uses_vcc, 1
	.set _Z6k_nodeILi0ELi0EEvPfS0_PDv2_DF16_PKiPKfS4_S0_S0_S4_S6_PKDv8_DF16_S6_S9_S6_S9_.uses_flat_scratch, 0
	.set _Z6k_nodeILi0ELi0EEvPfS0_PDv2_DF16_PKiPKfS4_S0_S0_S4_S6_PKDv8_DF16_S6_S9_S6_S9_.has_dyn_sized_stack, 0
	.set _Z6k_nodeILi0ELi0EEvPfS0_PDv2_DF16_PKiPKfS4_S0_S0_S4_S6_PKDv8_DF16_S6_S9_S6_S9_.has_recursion, 0
	.set _Z6k_nodeILi0ELi0EEvPfS0_PDv2_DF16_PKiPKfS4_S0_S0_S4_S6_PKDv8_DF16_S6_S9_S6_S9_.has_indirect_call, 0

	.text
	.protected	_Z6k_nodeILi1ELi0EEvPfS0_PDv2_DF16_PKiPKfS4_S0_S0_S4_S6_PKDv8_DF16_S6_S9_S6_S9_
	.globl	_Z6k_nodeILi1ELi0EEvPfS0_PDv2_DF16_PKiPKfS4_S0_S0_S4_S6_PKDv8_DF16_S6_S9_S6_S9_
	.p2align	8
	.type	_Z6k_nodeILi1ELi0EEvPfS0_PDv2_DF16_PKiPKfS4_S0_S0_S4_S6_PKDv8_DF16_S6_S9_S6_S9_,@function
_Z6k_nodeILi1ELi0EEvPfS0_PDv2_DF16_PKiPKfS4_S0_S0_S4_S6_PKDv8_DF16_S6_S9_S6_S9_:
	s_load_dwordx8 s[4:11], s[0:1], 0x40
	s_load_dwordx4 s[24:27], s[0:1], 0x18
	s_load_dwordx4 s[16:19], s[0:1], 0x60
	s_load_dwordx2 s[20:21], s[0:1], 0x70
	v_mov_b32_e32 v3, 0
	v_lshlrev_b32_e32 v176, 4, v0
	v_mov_b32_e32 v177, v3
	s_waitcnt lgkmcnt(0)
	v_lshl_add_u64 v[4:5], s[8:9], 0, v[176:177]
	s_movk_i32 s3, 0x1000
	v_add_co_u32_e32 v4, vcc, s3, v4
	global_load_dwordx4 v[46:49], v176, s[8:9]
	s_nop 0
	v_addc_co_u32_e32 v5, vcc, 0, v5, vcc
	global_load_dwordx4 v[50:53], v[4:5], off
	v_lshl_add_u64 v[4:5], s[16:17], 0, v[176:177]
	v_add_co_u32_e32 v4, vcc, 0x1000, v4
	s_load_dwordx4 s[12:15], s[0:1], 0x0
	s_nop 0
	v_addc_co_u32_e32 v5, vcc, 0, v5, vcc
	global_load_dwordx4 v[58:61], v176, s[16:17]
	global_load_dwordx4 v[54:57], v[4:5], off
	s_cmp_lg_u64 s[20:21], 0
	s_cselect_b64 s[8:9], -1, 0
	s_cmp_eq_u64 s[20:21], 0
	s_cbranch_scc1 .LBB8_2
	v_mov_b32_e32 v1, 0x1000
	v_lshl_or_b32 v1, v0, 4, v1
	global_load_dwordx4 v[168:171], v176, s[20:21]
	global_load_dwordx4 v[164:167], v1, s[20:21]
	s_branch .LBB8_3

.LBB8_3:
	v_lshrrev_b32_e32 v1, 6, v0
	v_lshl_or_b32 v172, s2, 2, v1
	v_and_b32_e32 v177, 31, v0
	v_lshlrev_b32_e32 v179, 5, v172
	v_or_b32_e32 v2, v179, v177
	v_min_i32_e32 v62, 0xc34f, v2
	v_ashrrev_i32_e32 v63, 31, v62
	v_lshl_add_u64 v[4:5], v[62:63], 2, s[4:5]
	global_load_dwordx2 v[174:175], v[4:5], off
	v_lshl_add_u64 v[218:219], v[62:63], 2, s[24:25]
	global_load_dword v218, v[218:219], off
	v_min_i32_e32 v4, 0x61a, v172
	v_lshlrev_b32_e32 v2, 5, v4
	v_sub_u32_e32 v2, 0xc350, v2
	v_min_u32_e32 v2, 32, v2
	v_add_u32_e32 v22, -1, v2
	v_ashrrev_i32_e32 v5, 31, v4
	v_lshlrev_b32_e32 v2, 2, v0
	v_and_b32_e32 v207, 60, v2
	v_lshlrev_b64 v[4:5], 13, v[4:5]
	v_bfe_u32 v206, v0, 4, 2
	v_lshl_or_b32 v4, v207, 2, v4
	s_waitcnt lgkmcnt(0)
	v_lshl_add_u64 v[6:7], s[12:13], 0, v[4:5]
	v_lshlrev_b32_e32 v2, 8, v206
	v_or_b32_e32 v204, 4, v206
	v_lshl_add_u64 v[8:9], v[6:7], 0, v[2:3]
	v_lshlrev_b32_e32 v10, 8, v204
	v_mov_b32_e32 v11, v3
	v_or_b32_e32 v203, 8, v206
	v_lshl_add_u64 v[12:13], v[6:7], 0, v[10:11]
	global_load_dwordx4 v[132:135], v[8:9], off
	global_load_dwordx4 v[136:139], v[12:13], off
	v_lshlrev_b32_e32 v8, 8, v203
	v_mov_b32_e32 v9, v3
	v_or_b32_e32 v202, 12, v206
	v_lshl_add_u64 v[12:13], v[6:7], 0, v[8:9]
	v_lshlrev_b32_e32 v14, 8, v202
	v_mov_b32_e32 v15, v3
	v_or_b32_e32 v201, 16, v206
	v_lshl_add_u64 v[16:17], v[6:7], 0, v[14:15]
	global_load_dwordx4 v[140:143], v[12:13], off
	global_load_dwordx4 v[144:147], v[16:17], off
	v_min_u32_e32 v12, v201, v22
	v_or_b32_e32 v200, 20, v206
	v_lshlrev_b32_e32 v12, 8, v12
	v_mov_b32_e32 v13, v3
	v_min_u32_e32 v18, v200, v22
	v_lshl_add_u64 v[16:17], v[6:7], 0, v[12:13]
	v_lshlrev_b32_e32 v18, 8, v18
	v_mov_b32_e32 v19, v3
	v_or_b32_e32 v199, 24, v206
	v_or_b32_e32 v198, 28, v206
	v_lshl_add_u64 v[20:21], v[6:7], 0, v[18:19]
	global_load_dwordx4 v[148:151], v[16:17], off
	global_load_dwordx4 v[152:155], v[20:21], off
	v_min_u32_e32 v16, v199, v22
	v_min_u32_e32 v22, v198, v22
	v_lshlrev_b32_e32 v16, 8, v16
	v_mov_b32_e32 v17, v3
	v_lshlrev_b32_e32 v22, 8, v22
	v_mov_b32_e32 v23, v3
	v_lshl_add_u64 v[4:5], s[14:15], 0, v[4:5]
	v_lshl_add_u64 v[20:21], v[6:7], 0, v[16:17]
	v_lshl_add_u64 v[6:7], v[6:7], 0, v[22:23]
	v_lshl_add_u64 v[2:3], v[4:5], 0, v[2:3]
	global_load_dwordx4 v[156:159], v[20:21], off
	global_load_dwordx4 v[160:163], v[6:7], off
	v_lshl_add_u64 v[6:7], v[4:5], 0, v[10:11]
	global_load_dwordx4 v[104:107], v[2:3], off
	global_load_dwordx4 v[100:103], v[6:7], off
	v_lshl_add_u64 v[2:3], v[4:5], 0, v[8:9]
	v_bfe_u32 v178, v0, 5, 1
	v_lshl_add_u64 v[6:7], v[4:5], 0, v[14:15]
	global_load_dwordx4 v[108:111], v[2:3], off
	global_load_dwordx4 v[112:115], v[6:7], off
	v_lshl_add_u64 v[2:3], v[4:5], 0, v[12:13]
	v_lshl_add_u64 v[6:7], v[4:5], 0, v[18:19]
	global_load_dwordx4 v[116:119], v[2:3], off
	global_load_dwordx4 v[120:123], v[6:7], off
	v_lshl_add_u64 v[2:3], v[4:5], 0, v[16:17]
	v_lshl_add_u64 v[4:5], v[4:5], 0, v[22:23]
	v_lshlrev_b32_e32 v173, 4, v178
	global_load_dwordx4 v[128:131], v[2:3], off
	global_load_dwordx4 v[124:127], v[4:5], off
	global_load_dwordx4 v[18:21], v173, s[10:11]
	global_load_dwordx4 v[22:25], v173, s[10:11] offset:32
	global_load_dwordx4 v[26:29], v173, s[10:11] offset:64
	global_load_dwordx4 v[30:33], v173, s[10:11] offset:96
	s_nop 0
	global_load_dwordx4 v[2:5], v173, s[10:11] offset:128
	global_load_dwordx4 v[6:9], v173, s[10:11] offset:160
	global_load_dwordx4 v[10:13], v173, s[10:11] offset:192
	global_load_dwordx4 v[14:17], v173, s[10:11] offset:224
	global_load_dwordx4 v[96:99], v173, s[18:19]
	global_load_dwordx4 v[92:95], v173, s[18:19] offset:32
	global_load_dwordx4 v[88:91], v173, s[18:19] offset:64
	global_load_dwordx4 v[84:87], v173, s[18:19] offset:96
	global_load_dwordx4 v[80:83], v173, s[18:19] offset:128
	global_load_dwordx4 v[42:45], v173, s[18:19] offset:160
	global_load_dwordx4 v[38:41], v173, s[18:19] offset:192
	global_load_dwordx4 v[34:37], v173, s[18:19] offset:224
	s_load_dwordx2 s[20:21], s[0:1], 0x10
	s_waitcnt vmcnt(36)
	ds_write_b128 v176, v[46:49] offset:34816
	s_waitcnt vmcnt(35)
	ds_write_b128 v176, v[50:53] offset:38912
	s_waitcnt vmcnt(34)
	ds_write_b128 v176, v[58:61] offset:43008
	v_cndmask_b32_e64 v46, 0, 1, s[8:9]
	v_cmp_ne_u32_e64 s[18:19], 1, v46
	s_andn2_b64 vcc, exec, s[8:9]
	s_waitcnt vmcnt(33)
	ds_write_b128 v176, v[54:57] offset:47104
	s_cbranch_vccnz .LBB8_5
	s_load_dwordx4 s[8:11], s[0:1], 0x18
	s_waitcnt lgkmcnt(0)
	s_nop 0
	s_nop 0
	v_lshlrev_b32_e32 v46, 2, v178
	v_mov_b32_e32 v47, 0
	v_lshlrev_b32_e32 v46, 2, v46
	s_waitcnt vmcnt(32)
	v_lshlrev_b32_e32 v48, 6, v218
	v_ashrrev_i32_e32 v49, 31, v48
	v_lshl_add_u64 v[48:49], v[48:49], 2, s[10:11]
	v_lshl_add_u64 v[46:47], v[48:49], 0, v[46:47]
	global_load_dwordx4 v[72:75], v[46:47], off
	global_load_dwordx4 v[76:79], v[46:47], off offset:32
	global_load_dwordx4 v[68:71], v[46:47], off offset:64
	global_load_dwordx4 v[64:67], v[46:47], off offset:96
	global_load_dwordx4 v[60:63], v[46:47], off offset:128
	global_load_dwordx4 v[56:59], v[46:47], off offset:160
	global_load_dwordx4 v[52:55], v[46:47], off offset:192
	global_load_dwordx4 v[48:51], v[46:47], off offset:224
	v_add_u32_e32 v46, 0x8800, v176
	ds_write_b128 v46, v[168:171] offset:16384
	ds_write_b128 v46, v[164:167] offset:20480
	s_branch .LBB8_6
.LBB8_5:
	s_waitcnt vmcnt(33)
.LBB8_6:
	s_nop 0
	v_ashrrev_i32_e32 v46, 5, v174
	v_add_u32_e32 v164, 1, v46
	v_sub_u32_e32 v209, 0xc350, v179
	v_lshlrev_b32_e32 v47, 5, v164
	v_cmp_gt_i32_e32 vcc, v209, v177
	v_cmp_lt_i32_e64 s[0:1], v47, v175
	v_ashrrev_i32_e32 v165, 31, v164
	v_lshlrev_b64 v[164:165], 6, v[164:165]
	s_and_b64 vcc, vcc, s[0:1]
	v_cndmask_b32_e32 v165, 0, v165, vcc
	v_cndmask_b32_e32 v164, 0, v164, vcc
	v_lshl_add_u64 v[164:165], v[164:165], 2, s[6:7]
	v_lshlrev_b32_e32 v194, 5, v178
	v_mov_b32_e32 v195, 0
	v_lshl_add_u64 v[196:197], v[164:165], 0, v[194:195]
	global_load_dwordx4 v[164:167], v[196:197], off
	global_load_dwordx4 v[168:171], v[196:197], off offset:16
	global_load_dwordx4 v[178:181], v[196:197], off offset:64
	global_load_dwordx4 v[182:185], v[196:197], off offset:80
	global_load_dwordx4 v[186:189], v[196:197], off offset:128
	global_load_dwordx4 v[190:193], v[196:197], off offset:144
	v_mul_u32_u24_e32 v208, 0x2200, v1
	v_mul_u32_u24_e32 v205, 0x110, v206
	v_lshlrev_b32_e32 v47, 2, v207
	v_add3_u32 v212, v208, v205, v47
	s_waitcnt vmcnt(37)
	ds_write_b128 v212, v[132:135]
	s_waitcnt vmcnt(36)
	ds_write_b128 v212, v[136:139] offset:1088
	s_waitcnt vmcnt(35)
	ds_write_b128 v212, v[140:143] offset:2176
	s_waitcnt vmcnt(34)
	ds_write_b128 v212, v[144:147] offset:3264
	s_waitcnt vmcnt(33)
	ds_write_b128 v212, v[148:151] offset:4352
	s_waitcnt vmcnt(32)
	ds_write_b128 v212, v[152:155] offset:5440
	s_waitcnt vmcnt(31)
	ds_write_b128 v212, v[156:159] offset:6528
	s_waitcnt vmcnt(30)
	ds_write_b128 v212, v[160:163] offset:7616
	global_load_dwordx4 v[132:135], v[196:197], off offset:208
	global_load_dwordx4 v[136:139], v[196:197], off offset:192
	s_movk_i32 s0, 0x2200
	v_mul_u32_u24_e32 v176, 0x110, v177
	v_mad_u32_u24 v211, v1, s0, v176
	v_add_u32_e32 v1, v211, v194
	s_waitcnt lgkmcnt(0)
	s_barrier
	ds_read_b128 v[140:143], v1
	ds_read_b128 v[144:147], v1 offset:16
	ds_read_b128 v[148:151], v1 offset:64
	ds_read_b128 v[152:155], v1 offset:80
	v_cmp_eq_u32_e64 s[0:1], v174, v175
	v_and_b32_e32 v210, 63, v0
	s_mov_b64 s[2:3], 0x200
	s_waitcnt vmcnt(7) lgkmcnt(3)
	v_add_f32_e32 v47, v140, v164
	v_add_f32_e32 v156, v141, v165
	v_add_f32_e32 v157, v142, v166
	v_add_f32_e32 v158, v143, v167
	s_waitcnt vmcnt(6) lgkmcnt(2)
	v_add_f32_e32 v159, v144, v168
	v_add_f32_e32 v160, v145, v169
	v_add_f32_e32 v161, v146, v170
	v_add_f32_e32 v162, v147, v171
	s_waitcnt vmcnt(5) lgkmcnt(1)
	v_add_f32_e32 v163, v148, v178
	v_add_f32_e32 v164, v149, v179
	v_cndmask_b32_e32 v47, v140, v47, vcc
	v_cndmask_b32_e32 v140, v141, v156, vcc
	v_cndmask_b32_e32 v141, v142, v157, vcc
	v_cndmask_b32_e32 v142, v143, v158, vcc
	v_cndmask_b32_e32 v143, v144, v159, vcc
	v_cndmask_b32_e32 v144, v145, v160, vcc
	v_cndmask_b32_e32 v145, v146, v161, vcc
	v_cndmask_b32_e32 v146, v147, v162, vcc
	v_cndmask_b32_e32 v147, v148, v163, vcc
	v_cndmask_b32_e32 v148, v149, v164, vcc
	v_cndmask_b32_e64 v161, v140, 0, s[0:1]
	v_cndmask_b32_e64 v162, v141, 0, s[0:1]
	v_cndmask_b32_e64 v163, v142, 0, s[0:1]
	v_cndmask_b32_e64 v164, v143, 0, s[0:1]
	ds_read_b128 v[140:143], v1 offset:128
	s_waitcnt vmcnt(4) lgkmcnt(1)
	v_add_f32_e32 v170, v154, v184
	v_cndmask_b32_e64 v160, v47, 0, s[0:1]
	v_cndmask_b32_e32 v47, v154, v170, vcc
	v_add_f32_e32 v165, v150, v180
	v_cndmask_b32_e64 v180, v47, 0, s[0:1]
	v_add_f32_e32 v47, v155, v185
	v_add_f32_e32 v166, v151, v181
	v_add_f32_e32 v167, v152, v182
	v_add_f32_e32 v168, v153, v183
	v_cndmask_b32_e32 v47, v155, v47, vcc
	v_cndmask_b32_e32 v149, v150, v165, vcc
	v_cndmask_b32_e32 v150, v151, v166, vcc
	v_cndmask_b32_e32 v151, v152, v167, vcc
	v_cndmask_b32_e32 v152, v153, v168, vcc
	v_cndmask_b32_e64 v165, v144, 0, s[0:1]
	v_cndmask_b32_e64 v166, v145, 0, s[0:1]
	v_cndmask_b32_e64 v167, v146, 0, s[0:1]
	v_cndmask_b32_e64 v168, v147, 0, s[0:1]
	v_cndmask_b32_e64 v181, v47, 0, s[0:1]
	ds_read_b128 v[144:147], v1 offset:144
	s_waitcnt vmcnt(3) lgkmcnt(1)
	v_add_f32_e32 v47, v140, v186
	v_cndmask_b32_e32 v47, v140, v47, vcc
	v_cndmask_b32_e64 v182, v47, 0, s[0:1]
	v_add_f32_e32 v47, v141, v187
	v_cndmask_b32_e32 v47, v141, v47, vcc
	v_cndmask_b32_e64 v183, v47, 0, s[0:1]
	v_add_f32_e32 v47, v142, v188
	v_cndmask_b32_e32 v47, v142, v47, vcc
	v_cndmask_b32_e64 v184, v47, 0, s[0:1]
	v_add_f32_e32 v47, v143, v189
	v_cndmask_b32_e32 v47, v143, v47, vcc
	v_cndmask_b32_e64 v185, v47, 0, s[0:1]
	s_waitcnt vmcnt(2) lgkmcnt(0)
	v_add_f32_e32 v47, v144, v190
	v_cndmask_b32_e32 v47, v144, v47, vcc
	v_cndmask_b32_e64 v186, v47, 0, s[0:1]
	v_add_f32_e32 v47, v145, v191
	ds_read_b128 v[140:143], v1 offset:192
	v_cndmask_b32_e32 v47, v145, v47, vcc
	v_cndmask_b32_e64 v187, v47, 0, s[0:1]
	v_add_f32_e32 v47, v146, v192
	v_cndmask_b32_e32 v47, v146, v47, vcc
	v_cndmask_b32_e64 v188, v47, 0, s[0:1]
	v_add_f32_e32 v47, v147, v193
	v_cndmask_b32_e32 v47, v147, v47, vcc
	ds_read_b128 v[144:147], v1 offset:208
	s_waitcnt vmcnt(0) lgkmcnt(1)
	v_add_f32_e32 v1, v140, v136
	v_cndmask_b32_e32 v1, v140, v1, vcc
	v_cndmask_b32_e64 v190, v1, 0, s[0:1]
	v_add_f32_e32 v1, v141, v137
	v_cndmask_b32_e32 v1, v141, v1, vcc
	v_cndmask_b32_e64 v191, v1, 0, s[0:1]
	v_add_f32_e32 v1, v142, v138
	v_cndmask_b32_e32 v1, v142, v1, vcc
	v_cndmask_b32_e64 v192, v1, 0, s[0:1]
	v_add_f32_e32 v1, v143, v139
	v_cndmask_b32_e32 v1, v143, v1, vcc
	v_cndmask_b32_e64 v193, v1, 0, s[0:1]
	s_waitcnt lgkmcnt(0)
	v_add_f32_e32 v1, v144, v132
	v_cndmask_b32_e32 v1, v144, v1, vcc
	v_cndmask_b32_e64 v194, v1, 0, s[0:1]
	v_add_f32_e32 v1, v145, v133
	v_cndmask_b32_e32 v1, v145, v1, vcc
	v_cndmask_b32_e64 v195, v1, 0, s[0:1]
	v_add_f32_e32 v1, v146, v134
	v_cndmask_b32_e32 v1, v146, v1, vcc
	v_cndmask_b32_e64 v196, v1, 0, s[0:1]
	v_add_f32_e32 v1, v147, v135
	v_cndmask_b32_e32 v1, v147, v1, vcc
	v_cndmask_b32_e64 v197, v1, 0, s[0:1]
	v_and_b32_e32 v1, 0xffffffe0, v174
	v_cndmask_b32_e64 v189, v47, 0, s[0:1]
	v_add_u32_e32 v47, 64, v1
	v_cndmask_b32_e64 v169, v148, 0, s[0:1]
	v_cndmask_b32_e64 v176, v149, 0, s[0:1]
	v_cndmask_b32_e64 v177, v150, 0, s[0:1]
	v_cndmask_b32_e64 v178, v151, 0, s[0:1]
	v_cndmask_b32_e64 v179, v152, 0, s[0:1]
	v_cmp_lt_i32_e64 s[0:1], v47, v175
	v_ashrrev_i32_e32 v47, 31, v46
	v_lshlrev_b64 v[46:47], 8, v[46:47]
	v_and_or_b32 v46, v0, 32, v46
	v_add_u32_e32 v174, 0x60, v1
	v_lshl_add_u64 v[0:1], s[6:7], 0, v[46:47]
	s_and_b64 s[0:1], vcc, s[0:1]
	v_lshl_add_u64 v[170:171], v[0:1], 0, s[2:3]
	s_mov_b64 s[2:3], 0x100
	s_branch .LBB8_9

	.amdhsa_kernel _Z6k_nodeILi1ELi0EEvPfS0_PDv2_DF16_PKiPKfS4_S0_S0_S4_S6_PKDv8_DF16_S6_S9_S6_S9_
		.amdhsa_group_segment_fixed_size 59392
		.amdhsa_private_segment_fixed_size 0
		.amdhsa_kernarg_size 120
		.amdhsa_user_sgpr_count 2
		.amdhsa_user_sgpr_dispatch_ptr 0
		.amdhsa_user_sgpr_queue_ptr 0
		.amdhsa_user_sgpr_kernarg_segment_ptr 1
		.amdhsa_user_sgpr_dispatch_id 0
		.amdhsa_user_sgpr_kernarg_preload_length 0
		.amdhsa_user_sgpr_kernarg_preload_offset 0
		.amdhsa_user_sgpr_private_segment_size 0
		.amdhsa_uses_dynamic_stack 0
		.amdhsa_enable_private_segment 0
		.amdhsa_system_sgpr_workgroup_id_x 1
		.amdhsa_system_sgpr_workgroup_id_y 0
		.amdhsa_system_sgpr_workgroup_id_z 0
		.amdhsa_system_sgpr_workgroup_info 0
		.amdhsa_system_vgpr_workitem_id 0
		.amdhsa_next_free_vgpr 220
		.amdhsa_next_free_sgpr 96
		.amdhsa_accum_offset 220
		.amdhsa_reserve_vcc 1
		.amdhsa_float_round_mode_32 0
		.amdhsa_float_round_mode_16_64 0
		.amdhsa_float_denorm_mode_32 3
		.amdhsa_float_denorm_mode_16_64 3
		.amdhsa_dx10_clamp 1
		.amdhsa_ieee_mode 1
		.amdhsa_fp16_overflow 0
		.amdhsa_tg_split 0
		.amdhsa_exception_fp_ieee_invalid_op 0
		.amdhsa_exception_fp_denorm_src 0
		.amdhsa_exception_fp_ieee_div_zero 0
		.amdhsa_exception_fp_ieee_overflow 0
		.amdhsa_exception_fp_ieee_underflow 0
		.amdhsa_exception_fp_ieee_inexact 0
		.amdhsa_exception_int_div_zero 0
	.end_amdhsa_kernel
	.text
.Lfunc_end8:
	.size	_Z6k_nodeILi1ELi0EEvPfS0_PDv2_DF16_PKiPKfS4_S0_S0_S4_S6_PKDv8_DF16_S6_S9_S6_S9_, .Lfunc_end8-_Z6k_nodeILi1ELi0EEvPfS0_PDv2_DF16_PKiPKfS4_S0_S0_S4_S6_PKDv8_DF16_S6_S9_S6_S9_
	.set _Z6k_nodeILi1ELi0EEvPfS0_PDv2_DF16_PKiPKfS4_S0_S0_S4_S6_PKDv8_DF16_S6_S9_S6_S9_.num_vgpr, 218
	.set _Z6k_nodeILi1ELi0EEvPfS0_PDv2_DF16_PKiPKfS4_S0_S0_S4_S6_PKDv8_DF16_S6_S9_S6_S9_.num_agpr, 0
	.set _Z6k_nodeILi1ELi0EEvPfS0_PDv2_DF16_PKiPKfS4_S0_S0_S4_S6_PKDv8_DF16_S6_S9_S6_S9_.numbered_sgpr, 24
	.set _Z6k_nodeILi1ELi0EEvPfS0_PDv2_DF16_PKiPKfS4_S0_S0_S4_S6_PKDv8_DF16_S6_S9_S6_S9_.num_named_barrier, 0
	.set _Z6k_nodeILi1ELi0EEvPfS0_PDv2_DF16_PKiPKfS4_S0_S0_S4_S6_PKDv8_DF16_S6_S9_S6_S9_.private_seg_size, 0
	.set _Z6k_nodeILi1ELi0EEvPfS0_PDv2_DF16_PKiPKfS4_S0_S0_S4_S6_PKDv8_DF16_S6_S9_S6_S9_.uses_vcc, 1
	.set _Z6k_nodeILi1ELi0EEvPfS0_PDv2_DF16_PKiPKfS4_S0_S0_S4_S6_PKDv8_DF16_S6_S9_S6_S9_.uses_flat_scratch, 0
	.set _Z6k_nodeILi1ELi0EEvPfS0_PDv2_DF16_PKiPKfS4_S0_S0_S4_S6_PKDv8_DF16_S6_S9_S6_S9_.has_dyn_sized_stack, 0
	.set _Z6k_nodeILi1ELi0EEvPfS0_PDv2_DF16_PKiPKfS4_S0_S0_S4_S6_PKDv8_DF16_S6_S9_S6_S9_.has_recursion, 0
	.set _Z6k_nodeILi1ELi0EEvPfS0_PDv2_DF16_PKiPKfS4_S0_S0_S4_S6_PKDv8_DF16_S6_S9_S6_S9_.has_indirect_call, 0

	.text
	.protected	_Z6k_nodeILi1ELi1EEvPfS0_PDv2_DF16_PKiPKfS4_S0_S0_S4_S6_PKDv8_DF16_S6_S9_S6_S9_
	.globl	_Z6k_nodeILi1ELi1EEvPfS0_PDv2_DF16_PKiPKfS4_S0_S0_S4_S6_PKDv8_DF16_S6_S9_S6_S9_
	.p2align	8
	.type	_Z6k_nodeILi1ELi1EEvPfS0_PDv2_DF16_PKiPKfS4_S0_S0_S4_S6_PKDv8_DF16_S6_S9_S6_S9_,@function

	.amdhsa_kernel _Z6k_nodeILi1ELi1EEvPfS0_PDv2_DF16_PKiPKfS4_S0_S0_S4_S6_PKDv8_DF16_S6_S9_S6_S9_
		.amdhsa_group_segment_fixed_size 59392
		.amdhsa_private_segment_fixed_size 0
		.amdhsa_kernarg_size 120
		.amdhsa_user_sgpr_count 2
		.amdhsa_user_sgpr_dispatch_ptr 0
		.amdhsa_user_sgpr_queue_ptr 0
		.amdhsa_user_sgpr_kernarg_segment_ptr 1
		.amdhsa_user_sgpr_dispatch_id 0
		.amdhsa_user_sgpr_kernarg_preload_length 0
		.amdhsa_user_sgpr_kernarg_preload_offset 0
		.amdhsa_user_sgpr_private_segment_size 0
		.amdhsa_uses_dynamic_stack 0
		.amdhsa_enable_private_segment 0
		.amdhsa_system_sgpr_workgroup_id_x 1
		.amdhsa_system_sgpr_workgroup_id_y 0
		.amdhsa_system_sgpr_workgroup_id_z 0
		.amdhsa_system_sgpr_workgroup_info 0
		.amdhsa_system_vgpr_workitem_id 0
		.amdhsa_next_free_vgpr 220
		.amdhsa_next_free_sgpr 96
		.amdhsa_accum_offset 220
		.amdhsa_reserve_vcc 1
		.amdhsa_float_round_mode_32 0
		.amdhsa_float_round_mode_16_64 0
		.amdhsa_float_denorm_mode_32 3
		.amdhsa_float_denorm_mode_16_64 3
		.amdhsa_dx10_clamp 1
		.amdhsa_ieee_mode 1
		.amdhsa_fp16_overflow 0
		.amdhsa_tg_split 0
		.amdhsa_exception_fp_ieee_invalid_op 0
		.amdhsa_exception_fp_denorm_src 0
		.amdhsa_exception_fp_ieee_div_zero 0
		.amdhsa_exception_fp_ieee_overflow 0
		.amdhsa_exception_fp_ieee_underflow 0
		.amdhsa_exception_fp_ieee_inexact 0
		.amdhsa_exception_int_div_zero 0
	.end_amdhsa_kernel
	.text
.Lfunc_end9:
	.size	_Z6k_nodeILi1ELi1EEvPfS0_PDv2_DF16_PKiPKfS4_S0_S0_S4_S6_PKDv8_DF16_S6_S9_S6_S9_, .Lfunc_end9-_Z6k_nodeILi1ELi1EEvPfS0_PDv2_DF16_PKiPKfS4_S0_S0_S4_S6_PKDv8_DF16_S6_S9_S6_S9_
	.set _Z6k_nodeILi1ELi1EEvPfS0_PDv2_DF16_PKiPKfS4_S0_S0_S4_S6_PKDv8_DF16_S6_S9_S6_S9_.num_vgpr, 220
	.set _Z6k_nodeILi1ELi1EEvPfS0_PDv2_DF16_PKiPKfS4_S0_S0_S4_S6_PKDv8_DF16_S6_S9_S6_S9_.num_agpr, 0
	.set _Z6k_nodeILi1ELi1EEvPfS0_PDv2_DF16_PKiPKfS4_S0_S0_S4_S6_PKDv8_DF16_S6_S9_S6_S9_.numbered_sgpr, 24
	.set _Z6k_nodeILi1ELi1EEvPfS0_PDv2_DF16_PKiPKfS4_S0_S0_S4_S6_PKDv8_DF16_S6_S9_S6_S9_.num_named_barrier, 0
	.set _Z6k_nodeILi1ELi1EEvPfS0_PDv2_DF16_PKiPKfS4_S0_S0_S4_S6_PKDv8_DF16_S6_S9_S6_S9_.private_seg_size, 0
	.set _Z6k_nodeILi1ELi1EEvPfS0_PDv2_DF16_PKiPKfS4_S0_S0_S4_S6_PKDv8_DF16_S6_S9_S6_S9_.uses_vcc, 1
	.set _Z6k_nodeILi1ELi1EEvPfS0_PDv2_DF16_PKiPKfS4_S0_S0_S4_S6_PKDv8_DF16_S6_S9_S6_S9_.uses_flat_scratch, 0
	.set _Z6k_nodeILi1ELi1EEvPfS0_PDv2_DF16_PKiPKfS4_S0_S0_S4_S6_PKDv8_DF16_S6_S9_S6_S9_.has_dyn_sized_stack, 0
	.set _Z6k_nodeILi1ELi1EEvPfS0_PDv2_DF16_PKiPKfS4_S0_S0_S4_S6_PKDv8_DF16_S6_S9_S6_S9_.has_recursion, 0
	.set _Z6k_nodeILi1ELi1EEvPfS0_PDv2_DF16_PKiPKfS4_S0_S0_S4_S6_PKDv8_DF16_S6_S9_S6_S9_.has_indirect_call, 0

amdhsa.kernels:
  - .agpr_count:     0
    .args:
      - .actual_access:  read_only
        .address_space:  global
        .offset:         0
        .size:           8
        .value_kind:     global_buffer
      - .actual_access:  write_only
        .address_space:  global
        .offset:         8
        .size:           8
        .value_kind:     global_buffer
      - .offset:         16
        .size:           288
        .value_kind:     by_value
      - .actual_access:  write_only
        .address_space:  global
        .offset:         304
        .size:           8
        .value_kind:     global_buffer
      - .actual_access:  write_only
        .address_space:  global
        .offset:         312
        .size:           8
        .value_kind:     global_buffer
    .group_segment_fixed_size: 1564
    .kernarg_segment_align: 8
    .kernarg_segment_size: 320
    .language:       OpenCL C
    .language_version:
      - 2
      - 0
    .max_flat_workgroup_size: 256
    .name:           _Z8k_bcountPKiPi8PrepArgsPDF16_S3_
    .private_segment_fixed_size: 0
    .sgpr_count:     26
    .sgpr_spill_count: 0
    .symbol:         _Z8k_bcountPKiPi8PrepArgsPDF16_S3_.kd
    .uniform_work_group_size: 1
    .uses_dynamic_stack: false
    .vgpr_count:     26
    .vgpr_spill_count: 0
    .wavefront_size: 64
  - .agpr_count:     0
    .args:
      - .actual_access:  read_only
        .address_space:  global
        .offset:         0
        .size:           8
        .value_kind:     global_buffer
      - .actual_access:  read_only
        .address_space:  global
        .offset:         8
        .size:           8
        .value_kind:     global_buffer
      - .actual_access:  read_only
        .address_space:  global
        .offset:         16
        .size:           8
        .value_kind:     global_buffer
      - .actual_access:  read_only
        .address_space:  global
        .offset:         24
        .size:           8
        .value_kind:     global_buffer
      - .actual_access:  write_only
        .address_space:  global
        .offset:         32
        .size:           8
        .value_kind:     global_buffer
      - .actual_access:  write_only
        .address_space:  global
        .offset:         40
        .size:           8
        .value_kind:     global_buffer
      - .actual_access:  write_only
        .address_space:  global
        .offset:         48
        .size:           8
        .value_kind:     global_buffer
    .group_segment_fixed_size: 19228
    .kernarg_segment_align: 8
    .kernarg_segment_size: 56
    .language:       OpenCL C
    .language_version:
      - 2
      - 0
    .max_flat_workgroup_size: 512
    .name:           _Z10k_bscatterPKfPKiS2_S2_PiP15HIP_vector_typeIfLj2EEPf
    .private_segment_fixed_size: 0
    .sgpr_count:     22
    .sgpr_spill_count: 0
    .symbol:         _Z10k_bscatterPKfPKiS2_S2_PiP15HIP_vector_typeIfLj2EEPf.kd
    .uniform_work_group_size: 1
    .uses_dynamic_stack: false
    .vgpr_count:     67
    .vgpr_spill_count: 0
    .wavefront_size: 64
  - .agpr_count:     0
    .args:
      - .actual_access:  read_only
        .address_space:  global
        .offset:         0
        .size:           8
        .value_kind:     global_buffer
      - .actual_access:  read_only
        .address_space:  global
        .offset:         8
        .size:           8
        .value_kind:     global_buffer
      - .actual_access:  read_only
        .address_space:  global
        .offset:         16
        .size:           8
        .value_kind:     global_buffer
      - .actual_access:  write_only
        .address_space:  global
        .offset:         24
        .size:           8
        .value_kind:     global_buffer
      - .actual_access:  write_only
        .address_space:  global
        .offset:         32
        .size:           8
        .value_kind:     global_buffer
    .group_segment_fixed_size: 1024
    .kernarg_segment_align: 8
    .kernarg_segment_size: 40
    .language:       OpenCL C
    .language_version:
      - 2
      - 0
    .max_flat_workgroup_size: 512
    .name:           _Z7k_bsortPK15HIP_vector_typeIfLj2EEPKiS4_PS_IfLj4EEPi
    .private_segment_fixed_size: 0
    .sgpr_count:     56
    .sgpr_spill_count: 0
    .symbol:         _Z7k_bsortPK15HIP_vector_typeIfLj2EEPKiS4_PS_IfLj4EEPi.kd
    .uniform_work_group_size: 1
    .uses_dynamic_stack: false
    .vgpr_count:     64
    .vgpr_spill_count: 0
    .wavefront_size: 64
  - .agpr_count:     0
    .args:
      - .actual_access:  read_only
        .address_space:  global
        .offset:         0
        .size:           8
        .value_kind:     global_buffer
      - .actual_access:  read_only
        .address_space:  global
        .offset:         8
        .size:           8
        .value_kind:     global_buffer
      - .actual_access:  read_only
        .address_space:  global
        .offset:         16
        .size:           8
        .value_kind:     global_buffer
      - .actual_access:  read_only
        .address_space:  global
        .offset:         24
        .size:           8
        .value_kind:     global_buffer
      - .actual_access:  read_only
        .address_space:  global
        .offset:         32
        .size:           8
        .value_kind:     global_buffer
      - .actual_access:  read_only
        .address_space:  global
        .offset:         40
        .size:           8
        .value_kind:     global_buffer
      - .actual_access:  write_only
        .address_space:  global
        .offset:         48
        .size:           8
        .value_kind:     global_buffer
      - .actual_access:  write_only
        .address_space:  global
        .offset:         56
        .size:           8
        .value_kind:     global_buffer
      - .offset:         64
        .size:           4
        .value_kind:     hidden_block_count_x
      - .offset:         68
        .size:           4
        .value_kind:     hidden_block_count_y
      - .offset:         72
        .size:           4
        .value_kind:     hidden_block_count_z
      - .offset:         76
        .size:           2
        .value_kind:     hidden_group_size_x
      - .offset:         78
        .size:           2
        .value_kind:     hidden_group_size_y
      - .offset:         80
        .size:           2
        .value_kind:     hidden_group_size_z
      - .offset:         82
        .size:           2
        .value_kind:     hidden_remainder_x
      - .offset:         84
        .size:           2
        .value_kind:     hidden_remainder_y
      - .offset:         86
        .size:           2
        .value_kind:     hidden_remainder_z
      - .offset:         104
        .size:           8
        .value_kind:     hidden_global_offset_x
      - .offset:         112
        .size:           8
        .value_kind:     hidden_global_offset_y
      - .offset:         120
        .size:           8
        .value_kind:     hidden_global_offset_z
      - .offset:         128
        .size:           2
        .value_kind:     hidden_grid_dims
    .group_segment_fixed_size: 31488
    .kernarg_segment_align: 8
    .kernarg_segment_size: 320
    .language:       OpenCL C
    .language_version:
      - 2
      - 0
    .max_flat_workgroup_size: 256
    .name:           _Z7k_edge0PK15HIP_vector_typeIfLj4EEPKDv8_DF16_S5_PKfS7_S7_PfS8_
    .private_segment_fixed_size: 0
    .sgpr_count:     59
    .sgpr_spill_count: 0
    .symbol:         _Z7k_edge0PK15HIP_vector_typeIfLj4EEPKDv8_DF16_S5_PKfS7_S7_PfS8_.kd
    .uniform_work_group_size: 1
    .uses_dynamic_stack: false
    .vgpr_count:     94
    .vgpr_spill_count: 0
    .wavefront_size: 64
  - .agpr_count:     0
    .args:
      - .actual_access:  read_only
        .address_space:  global
        .offset:         0
        .size:           8
        .value_kind:     global_buffer
      - .actual_access:  read_only
        .address_space:  global
        .offset:         8
        .size:           8
        .value_kind:     global_buffer
      - .actual_access:  read_only
        .address_space:  global
        .offset:         16
        .size:           8
        .value_kind:     global_buffer
      - .actual_access:  read_only
        .address_space:  global
        .offset:         24
        .size:           8
        .value_kind:     global_buffer
      - .actual_access:  read_only
        .address_space:  global
        .offset:         32
        .size:           8
        .value_kind:     global_buffer
      - .actual_access:  read_only
        .address_space:  global
        .offset:         40
        .size:           8
        .value_kind:     global_buffer
      - .address_space:  global
        .offset:         48
        .size:           8
        .value_kind:     global_buffer
      - .actual_access:  write_only
        .address_space:  global
        .offset:         56
        .size:           8
        .value_kind:     global_buffer
      - .actual_access:  write_only
        .address_space:  global
        .offset:         64
        .size:           8
        .value_kind:     global_buffer
      - .offset:         72
        .size:           4
        .value_kind:     hidden_block_count_x
      - .offset:         76
        .size:           4
        .value_kind:     hidden_block_count_y
      - .offset:         80
        .size:           4
        .value_kind:     hidden_block_count_z
      - .offset:         84
        .size:           2
        .value_kind:     hidden_group_size_x
      - .offset:         86
        .size:           2
        .value_kind:     hidden_group_size_y
      - .offset:         88
        .size:           2
        .value_kind:     hidden_group_size_z
      - .offset:         90
        .size:           2
        .value_kind:     hidden_remainder_x
      - .offset:         92
        .size:           2
        .value_kind:     hidden_remainder_y
      - .offset:         94
        .size:           2
        .value_kind:     hidden_remainder_z
      - .offset:         112
        .size:           8
        .value_kind:     hidden_global_offset_x
      - .offset:         120
        .size:           8
        .value_kind:     hidden_global_offset_y
      - .offset:         128
        .size:           8
        .value_kind:     hidden_global_offset_z
      - .offset:         136
        .size:           2
        .value_kind:     hidden_grid_dims
    .group_segment_fixed_size: 31488
    .kernarg_segment_align: 8
    .kernarg_segment_size: 328
    .language:       OpenCL C
    .language_version:
      - 2
      - 0
    .max_flat_workgroup_size: 256
    .name:           _Z7k_edge1PK15HIP_vector_typeIfLj4EEPKDv8_DF16_S5_PKfS7_S7_PKDv2_DF16_PfSB_
    .private_segment_fixed_size: 0
    .sgpr_count:     56
    .sgpr_spill_count: 0
    .symbol:         _Z7k_edge1PK15HIP_vector_typeIfLj4EEPKDv8_DF16_S5_PKfS7_S7_PKDv2_DF16_PfSB_.kd
    .uniform_work_group_size: 1
    .uses_dynamic_stack: false
    .vgpr_count:     124
    .vgpr_spill_count: 0
    .wavefront_size: 64
  - .agpr_count:     0
    .args:
      - .actual_access:  read_only
        .address_space:  global
        .offset:         0
        .size:           8
        .value_kind:     global_buffer
      - .actual_access:  read_only
        .address_space:  global
        .offset:         8
        .size:           8
        .value_kind:     global_buffer
      - .address_space:  global
        .offset:         16
        .size:           8
        .value_kind:     global_buffer
      - .address_space:  global
        .offset:         24
        .size:           8
        .value_kind:     global_buffer
    .group_segment_fixed_size: 0
    .kernarg_segment_align: 8
    .kernarg_segment_size: 32
    .language:       OpenCL C
    .language_version:
      - 2
      - 0
    .max_flat_workgroup_size: 256
    .name:           _Z6k_poolPKfPKiPfS3_
    .private_segment_fixed_size: 0
    .sgpr_count:     20
    .sgpr_spill_count: 0
    .symbol:         _Z6k_poolPKfPKiPfS3_.kd
    .uniform_work_group_size: 1
    .uses_dynamic_stack: false
    .vgpr_count:     16
    .vgpr_spill_count: 0
    .wavefront_size: 64
  - .agpr_count:     0
    .args:
      - .actual_access:  read_only
        .address_space:  global
        .offset:         0
        .size:           8
        .value_kind:     global_buffer
      - .actual_access:  read_only
        .address_space:  global
        .offset:         8
        .size:           8
        .value_kind:     global_buffer
      - .actual_access:  read_only
        .address_space:  global
        .offset:         16
        .size:           8
        .value_kind:     global_buffer
      - .actual_access:  read_only
        .address_space:  global
        .offset:         24
        .size:           8
        .value_kind:     global_buffer
      - .actual_access:  read_only
        .address_space:  global
        .offset:         32
        .size:           8
        .value_kind:     global_buffer
      - .actual_access:  read_only
        .address_space:  global
        .offset:         40
        .size:           8
        .value_kind:     global_buffer
      - .actual_access:  write_only
        .address_space:  global
        .offset:         48
        .size:           8
        .value_kind:     global_buffer
    .group_segment_fixed_size: 20480
    .kernarg_segment_align: 8
    .kernarg_segment_size: 56
    .language:       OpenCL C
    .language_version:
      - 2
      - 0
    .max_flat_workgroup_size: 64
    .name:           _Z7k_finalPKfS0_S0_S0_S0_S0_Pf
    .private_segment_fixed_size: 0
    .sgpr_count:     42
    .sgpr_spill_count: 0
    .symbol:         _Z7k_finalPKfS0_S0_S0_S0_S0_Pf.kd
    .uniform_work_group_size: 1
    .uses_dynamic_stack: false
    .vgpr_count:     144
    .vgpr_spill_count: 0
    .wavefront_size: 64
  - .agpr_count:     0
    .args:
      - .actual_access:  read_only
        .address_space:  global
        .offset:         0
        .size:           8
        .value_kind:     global_buffer
      - .address_space:  global
        .offset:         8
        .size:           8
        .value_kind:     global_buffer
      - .address_space:  global
        .offset:         16
        .size:           8
        .value_kind:     global_buffer
      - .actual_access:  read_only
        .address_space:  global
        .offset:         24
        .size:           8
        .value_kind:     global_buffer
      - .actual_access:  read_only
        .address_space:  global
        .offset:         32
        .size:           8
        .value_kind:     global_buffer
      - .actual_access:  read_only
        .address_space:  global
        .offset:         40
        .size:           8
        .value_kind:     global_buffer
      - .actual_access:  read_only
        .address_space:  global
        .offset:         48
        .size:           8
        .value_kind:     global_buffer
      - .actual_access:  read_only
        .address_space:  global
        .offset:         56
        .size:           8
        .value_kind:     global_buffer
      - .actual_access:  read_only
        .address_space:  global
        .offset:         64
        .size:           8
        .value_kind:     global_buffer
      - .actual_access:  read_only
        .address_space:  global
        .offset:         72
        .size:           8
        .value_kind:     global_buffer
      - .actual_access:  read_only
        .address_space:  global
        .offset:         80
        .size:           8
        .value_kind:     global_buffer
      - .actual_access:  read_only
        .address_space:  global
        .offset:         88
        .size:           8
        .value_kind:     global_buffer
      - .actual_access:  read_only
        .address_space:  global
        .offset:         96
        .size:           8
        .value_kind:     global_buffer
      - .actual_access:  read_only
        .address_space:  global
        .offset:         104
        .size:           8
        .value_kind:     global_buffer
      - .actual_access:  read_only
        .address_space:  global
        .offset:         112
        .size:           8
        .value_kind:     global_buffer
    .group_segment_fixed_size: 59392
    .kernarg_segment_align: 8
    .kernarg_segment_size: 120
    .language:       OpenCL C
    .language_version:
      - 2
      - 0
    .max_flat_workgroup_size: 256
    .name:           _Z6k_nodeILi0ELi0EEvPfS0_PDv2_DF16_PKiPKfS4_S0_S0_S4_S6_PKDv8_DF16_S6_S9_S6_S9_
    .private_segment_fixed_size: 0
    .sgpr_count:     30
    .sgpr_spill_count: 0
    .symbol:         _Z6k_nodeILi0ELi0EEvPfS0_PDv2_DF16_PKiPKfS4_S0_S0_S4_S6_PKDv8_DF16_S6_S9_S6_S9_.kd
    .uniform_work_group_size: 1
    .uses_dynamic_stack: false
    .vgpr_count:     154
    .vgpr_spill_count: 0
    .wavefront_size: 64
  - .agpr_count:     0
    .args:
      - .actual_access:  read_only
        .address_space:  global
        .offset:         0
        .size:           8
        .value_kind:     global_buffer
      - .address_space:  global
        .offset:         8
        .size:           8
        .value_kind:     global_buffer
      - .address_space:  global
        .offset:         16
        .size:           8
        .value_kind:     global_buffer
      - .actual_access:  read_only
        .address_space:  global
        .offset:         24
        .size:           8
        .value_kind:     global_buffer
      - .actual_access:  read_only
        .address_space:  global
        .offset:         32
        .size:           8
        .value_kind:     global_buffer
      - .actual_access:  read_only
        .address_space:  global
        .offset:         40
        .size:           8
        .value_kind:     global_buffer
      - .actual_access:  read_only
        .address_space:  global
        .offset:         48
        .size:           8
        .value_kind:     global_buffer
      - .actual_access:  read_only
        .address_space:  global
        .offset:         56
        .size:           8
        .value_kind:     global_buffer
      - .actual_access:  read_only
        .address_space:  global
        .offset:         64
        .size:           8
        .value_kind:     global_buffer
      - .actual_access:  read_only
        .address_space:  global
        .offset:         72
        .size:           8
        .value_kind:     global_buffer
      - .actual_access:  read_only
        .address_space:  global
        .offset:         80
        .size:           8
        .value_kind:     global_buffer
      - .actual_access:  read_only
        .address_space:  global
        .offset:         88
        .size:           8
        .value_kind:     global_buffer
      - .actual_access:  read_only
        .address_space:  global
        .offset:         96
        .size:           8
        .value_kind:     global_buffer
      - .actual_access:  read_only
        .address_space:  global
        .offset:         104
        .size:           8
        .value_kind:     global_buffer
      - .actual_access:  read_only
        .address_space:  global
        .offset:         112
        .size:           8
        .value_kind:     global_buffer
    .group_segment_fixed_size: 59392
    .kernarg_segment_align: 8
    .kernarg_segment_size: 120
    .language:       OpenCL C
    .language_version:
      - 2
      - 0
    .max_flat_workgroup_size: 256
    .name:           _Z6k_nodeILi1ELi0EEvPfS0_PDv2_DF16_PKiPKfS4_S0_S0_S4_S6_PKDv8_DF16_S6_S9_S6_S9_
    .private_segment_fixed_size: 0
    .sgpr_count:     30
    .sgpr_spill_count: 0
    .symbol:         _Z6k_nodeILi1ELi0EEvPfS0_PDv2_DF16_PKiPKfS4_S0_S0_S4_S6_PKDv8_DF16_S6_S9_S6_S9_.kd
    .uniform_work_group_size: 1
    .uses_dynamic_stack: false
    .vgpr_count:     220
    .vgpr_spill_count: 0
    .wavefront_size: 64
  - .agpr_count:     0
    .args:
      - .actual_access:  read_only
        .address_space:  global
        .offset:         0
        .size:           8
        .value_kind:     global_buffer
      - .actual_access:  read_only
        .address_space:  global
        .offset:         8
        .size:           8
        .value_kind:     global_buffer
      - .address_space:  global
        .offset:         16
        .size:           8
        .value_kind:     global_buffer
      - .actual_access:  read_only
        .address_space:  global
        .offset:         24
        .size:           8
        .value_kind:     global_buffer
      - .actual_access:  read_only
        .address_space:  global
        .offset:         32
        .size:           8
        .value_kind:     global_buffer
      - .actual_access:  read_only
        .address_space:  global
        .offset:         40
        .size:           8
        .value_kind:     global_buffer
      - .address_space:  global
        .offset:         48
        .size:           8
        .value_kind:     global_buffer
      - .address_space:  global
        .offset:         56
        .size:           8
        .value_kind:     global_buffer
      - .actual_access:  read_only
        .address_space:  global
        .offset:         64
        .size:           8
        .value_kind:     global_buffer
      - .actual_access:  read_only
        .address_space:  global
        .offset:         72
        .size:           8
        .value_kind:     global_buffer
      - .actual_access:  read_only
        .address_space:  global
        .offset:         80
        .size:           8
        .value_kind:     global_buffer
      - .actual_access:  read_only
        .address_space:  global
        .offset:         88
        .size:           8
        .value_kind:     global_buffer
      - .actual_access:  read_only
        .address_space:  global
        .offset:         96
        .size:           8
        .value_kind:     global_buffer
      - .actual_access:  read_only
        .address_space:  global
        .offset:         104
        .size:           8
        .value_kind:     global_buffer
      - .actual_access:  read_only
        .address_space:  global
        .offset:         112
        .size:           8
        .value_kind:     global_buffer
    .group_segment_fixed_size: 59392
    .kernarg_segment_align: 8
    .kernarg_segment_size: 120
    .language:       OpenCL C
    .language_version:
      - 2
      - 0
    .max_flat_workgroup_size: 256
    .name:           _Z6k_nodeILi1ELi1EEvPfS0_PDv2_DF16_PKiPKfS4_S0_S0_S4_S6_PKDv8_DF16_S6_S9_S6_S9_
    .private_segment_fixed_size: 0
    .sgpr_count:     30
    .sgpr_spill_count: 0
    .symbol:         _Z6k_nodeILi1ELi1EEvPfS0_PDv2_DF16_PKiPKfS4_S0_S0_S4_S6_PKDv8_DF16_S6_S9_S6_S9_.kd
    .uniform_work_group_size: 1
    .uses_dynamic_stack: false
    .vgpr_count:     220
    .vgpr_spill_count: 0
    .wavefront_size: 64
